# v62 plus compress-stage-1 GEMM split in two K halves over 32 workgroups (f32 partials exchanged through the dead nsaacc buffer, flag release/acquire); token-shift and V-transpose work moved to workgro
# speedup vs baseline: 1.0046x; 1.0046x over previous
; #define PHASE_END   } if (gp + 1 < hi) xcd_barrier(bar); } ++gp;
; #define RELAUNDER() do { asm volatile("" : "+v"(pc.tid), "+s"(pc.bid)); pc.lane = pc.tid & 63; pc.wave = __builtin_amdgcn_readfirstlane(pc.tid >> 6); } while (0)
; __device__ __forceinline__ void phase_lora_a(const Ctx& c, const Args& a, int layer, const bf16_t* proj, bf16_t* alora) {
;     ...
;     for (int t = c.bid * 16 + rloc; t < T; t += c.G * 16) {
; __global__ void __launch_bounds__(512, 2) fwd_kernel(Args args) {
;     ...
;             PHASE_BEGIN(16) {
;                 { pg8::Gemm g{proj, wb + WB_W1T, 16 * PLD, 2048, 2048, (unsigned)PLD * 2}; pg8::Sched S; S.init(16, 1, c.G, c.bid, 1, 0, 0, 0, 0); S.mode = 1;
;                   pg8::EpiCmp1 E{hidb, (const float*)(wb + WB_BH)}; pg8::gemm_phase(c.lds, c.tid, g, S, E); }
;                 RELAUNDER();
;                 if (c.bid >= 16) { Ctx cv = c; cv.bid = c.bid - 16; cv.G = c.G - 16; phase_lora_a(cv, args, layer, proj, alora); vt_transpose(cv, proj, vtb); } } PHASE_END
.LBB0_75:
	s_add_u32 s2, s76, 0x10000
	s_addc_u32 s3, s77, 0
	s_add_u32 s78, s76, 0x68e0000
	v_writelane_b32 v251, s2, 6
	s_addc_u32 s79, s77, 0
	s_load_dwordx2 s[0:1], s[0:1], 0xf0
	v_writelane_b32 v251, s3, 7
	s_add_u32 s2, s76, 0x2650000
	v_writelane_b32 v251, s2, 8
	s_addc_u32 s2, s77, 0
	v_writelane_b32 v251, s2, 9
	s_add_u32 s2, s76, 0x2450000
	v_writelane_b32 v251, s2, 10
	s_addc_u32 s2, s77, 0
	v_writelane_b32 v251, s2, 11
	s_add_u32 s2, s76, 0x2390000
	s_addc_u32 s3, s77, 0
	v_writelane_b32 v251, s2, 12
	v_mbcnt_lo_u32_b32 v2, -1, 0
	s_mov_b32 s43, 0
	v_writelane_b32 v251, s3, 13
	s_add_u32 s2, s76, 0x1e10000
	s_addc_u32 s3, s77, 0
	v_writelane_b32 v251, s2, 14
	s_mov_b32 s63, 0x20000
	s_brev_b32 s62, -2
	v_writelane_b32 v251, s3, 15
	s_add_u32 s2, s76, 0x1310000
	s_addc_u32 s3, s77, 0
	v_writelane_b32 v251, s2, 16
	v_mov_b32_e32 v186, 0x3a27c5ac
	v_mov_b32_e32 v234, 0x358637bd
	v_writelane_b32 v251, s3, 17
	s_add_u32 s2, s76, 0x1110000
	s_addc_u32 s3, s77, 0
	v_writelane_b32 v251, s2, 18
	v_mov_b32_e32 v188, 0x41b17218
	v_mov_b32_e32 v190, 0xf149f2ca
	v_writelane_b32 v251, s3, 19
	s_add_u32 s2, s76, 0xe10000
	v_writelane_b32 v251, s2, 20
	s_addc_u32 s2, s77, 0
	v_writelane_b32 v251, s2, 21
	s_lshl_b32 s2, s74, 1
	v_writelane_b32 v251, s2, 22
	s_add_u32 s2, s76, 0x200
	s_addc_u32 s3, s77, 0
	v_writelane_b32 v251, s2, 23
	v_mbcnt_hi_u32_b32 v244, -1, v2
	v_mov_b32_e32 v194, 0xff800000
	v_writelane_b32 v251, s3, 24
	s_add_u32 s2, s76, 0x1000
	s_addc_u32 s3, s77, 0
	v_writelane_b32 v251, s2, 25
	s_movk_i32 s96, 0x7f
	s_movk_i32 s23, 0x100
	v_writelane_b32 v251, s3, 26
	s_add_u32 s2, s76, 0x1100
	s_addc_u32 s3, s77, 0
	v_writelane_b32 v251, s2, 27
	s_movk_i32 s67, 0x90
	s_movk_i32 s97, 0x1000
	v_writelane_b32 v251, s3, 28
	s_add_u32 s2, s76, 0x1200
	s_addc_u32 s3, s77, 0
	v_writelane_b32 v251, s2, 29
	s_mov_b32 s16, 1
	s_mov_b32 s33, 0x800000
	v_writelane_b32 v251, s3, 30
	s_add_u32 s2, s76, 0x1300
	s_addc_u32 s3, s77, 0
	v_writelane_b32 v251, s2, 31
	s_cmp_eq_u32 s24, 15
	s_mov_b32 s72, 0xf149f2ca
	v_writelane_b32 v251, s3, 32
	s_cselect_b64 s[2:3], -1, 0
	v_writelane_b32 v251, s2, 33
	s_cmp_eq_u32 s24, 14
	s_movk_i32 s73, 0x4c
	v_writelane_b32 v251, s3, 34
	s_cselect_b64 s[2:3], -1, 0
	v_writelane_b32 v251, s2, 35
	s_cmp_eq_u32 s24, 13
	s_movk_i32 s25, 0x315
	v_writelane_b32 v251, s3, 36
	s_cselect_b64 s[2:3], -1, 0
	v_writelane_b32 v251, s2, 37
	s_cmp_eq_u32 s24, 12
	s_mov_b32 s30, 0xefa18f08
	v_writelane_b32 v251, s3, 38
	s_cselect_b64 s[2:3], -1, 0
	v_writelane_b32 v251, s2, 39
	s_cmp_eq_u32 s24, 11
	s_mov_b32 s31, 0xe1fc780f
	v_writelane_b32 v251, s3, 40
	s_cselect_b64 s[2:3], -1, 0
	v_writelane_b32 v251, s2, 41
	s_cmp_eq_u32 s24, 10
	s_movk_i32 s18, 0xfb78
	v_writelane_b32 v251, s3, 42
	s_cselect_b64 s[2:3], -1, 0
	v_writelane_b32 v251, s2, 43
	s_cmp_eq_u32 s24, 9
	s_movk_i32 s19, 0x380
	v_writelane_b32 v251, s3, 44
	s_cselect_b64 s[2:3], -1, 0
	v_writelane_b32 v251, s2, 45
	s_cmp_eq_u32 s24, 8
	s_movk_i32 s34, 0x3f0
	v_writelane_b32 v251, s3, 46
	s_cselect_b64 s[2:3], -1, 0
	v_writelane_b32 v251, s2, 47
	s_cmp_eq_u32 s24, 7
	s_movk_i32 s35, 0x101f
	v_writelane_b32 v251, s3, 48
	s_cselect_b64 s[2:3], -1, 0
	v_writelane_b32 v251, s2, 49
	s_cmp_eq_u32 s24, 6
	s_mov_b64 s[44:45], 0x80
	v_writelane_b32 v251, s3, 50
	s_cselect_b64 s[2:3], -1, 0
	v_writelane_b32 v251, s2, 51
	s_cmp_eq_u32 s24, 5
	s_nop 0
	v_writelane_b32 v251, s3, 52
	s_cselect_b64 s[2:3], -1, 0
	v_writelane_b32 v251, s2, 53
	s_cmp_eq_u32 s24, 4
	s_nop 0
	v_writelane_b32 v251, s3, 54
	s_cselect_b64 s[2:3], -1, 0
	v_writelane_b32 v251, s2, 55
	s_cmp_eq_u32 s24, 3
	s_nop 0
	v_writelane_b32 v251, s3, 56
	s_cselect_b64 s[2:3], -1, 0
	v_writelane_b32 v251, s2, 57
	s_cmp_eq_u32 s24, 2
	s_nop 0
	v_writelane_b32 v251, s3, 58
	s_cselect_b64 s[2:3], -1, 0
	v_writelane_b32 v251, s2, 59
	s_cmp_eq_u32 s24, 1
	s_nop 0
	v_writelane_b32 v251, s3, 60
	s_cselect_b64 s[2:3], -1, 0
	v_writelane_b32 v251, s2, 61
	s_cmp_eq_u32 s24, 0
	s_nop 0
	v_writelane_b32 v251, s3, 62
	s_cselect_b64 s[2:3], -1, 0
	v_writelane_b32 v251, s2, 63
	s_nop 1
	v_writelane_b32 v252, s3, 0
	s_lshl_b32 s2, s24, 8
	s_add_u32 s2, s76, s2
	s_addc_u32 s3, s77, 0
	s_add_u32 s4, s2, 0x1400
	s_addc_u32 s5, s3, 0
	v_writelane_b32 v252, s4, 1
	s_add_u32 s2, s2, 0x2400
	s_addc_u32 s3, s3, 0
	v_writelane_b32 v252, s5, 2
	v_writelane_b32 v252, s2, 3
	s_mov_b32 s24, 0xbfb8aa3b
	s_nop 0
	v_writelane_b32 v252, s3, 4
	s_add_u32 s2, s76, 0x3400
	s_addc_u32 s3, s77, 0
	v_writelane_b32 v252, s2, 5
	s_nop 1
	v_writelane_b32 v252, s3, 6
	s_add_u32 s2, s76, 0x3500
	s_addc_u32 s3, s77, 0
	v_writelane_b32 v252, s2, 7
	s_nop 1
	v_writelane_b32 v252, s3, 8
	s_add_i32 s2, s74, -1
	v_writelane_b32 v252, s2, 9
	s_add_u32 s2, s76, 0x2690000
	s_addc_u32 s3, s77, 0
	v_writelane_b32 v252, s2, 10
	s_nop 1
	v_writelane_b32 v252, s3, 11
	s_add_u32 s2, s76, 0x26c0000
	s_addc_u32 s3, s77, 0
	s_add_u32 s80, s76, 0x7f00000
	v_writelane_b32 v252, s2, 12
	s_addc_u32 s81, s77, 0
	s_mov_b32 s8, s80
	v_writelane_b32 v252, s3, 13
	s_add_u32 s2, s76, 0xff00000
	v_writelane_b32 v252, s2, 14
	s_addc_u32 s2, s77, 0
	s_ashr_i32 s75, s74, 31
	v_writelane_b32 v252, s2, 15
	s_add_u32 s2, s76, 0x67e0000
	s_addc_u32 s3, s77, 0
	v_writelane_b32 v252, s2, 16
	s_nop 1
	v_writelane_b32 v252, s3, 17
	s_add_i32 s2, s74, -32
	s_add_u32 s4, s76, 0x6b00000
	s_addc_u32 s5, s77, 0
	v_writelane_b32 v252, s4, 18
	s_nop 1
	v_writelane_b32 v252, s5, 19
	s_lshl_b32 s4, s2, 4
	s_add_u32 s82, s76, 0x7300000
	s_addc_u32 s83, s77, 0
	s_add_u32 s84, s76, 0x1cf00000
	s_addc_u32 s85, s77, 0
	v_writelane_b32 v252, s2, 20
	s_add_u32 s2, s76, 0x6760000
	s_addc_u32 s3, s77, 0
; #define LAS __attribute__((address_space(3)))
; #define PHASE_END   } if (gp + 1 < hi) xcd_barrier(bar); } ++gp;
; __device__ __forceinline__ void vt_transpose(const Ctx& c, const bf16_t* proj, bf16_t* vt) {
;     LAS bf16_t* tl = (LAS bf16_t*)c.lds;
;     for (int it = c.bid; it < 3 * 2 * 256; it += c.G) {
; __global__ void __launch_bounds__(512, 2) fwd_kernel(Args args) {
;     ...
;                 if (c.bid >= 16) { Ctx cv = c; cv.bid = c.bid - 16; cv.G = c.G - 16; phase_lora_a(cv, args, layer, proj, alora); vt_transpose(cv, proj, vtb); } } PHASE_END
	s_add_u32 s86, s76, 0x67a0000
	s_addc_u32 s87, s77, 0
	s_add_u32 s88, s76, 0x1df00000
	s_addc_u32 s89, s77, 0
	s_add_u32 s90, s76, 0x1ef00000
	s_addc_u32 s91, s77, 0
	s_add_u32 s40, s76, 0x15f00000
	v_writelane_b32 v252, s2, 21
	s_addc_u32 s41, s77, 0
	s_mov_b32 s68, s40
	v_writelane_b32 v252, s3, 22
	s_add_u32 s2, s76, 0x66e0000
	v_writelane_b32 v252, s2, 23
	s_addc_u32 s2, s77, 0
	v_writelane_b32 v252, s2, 24
	s_add_u32 s2, s76, 0x1af00000
	s_addc_u32 s3, s77, 0
	v_writelane_b32 v252, s2, 25
	s_nop 1
	v_writelane_b32 v252, s3, 26
	s_add_u32 s2, s76, 0x19f00000
	v_writelane_b32 v252, s2, 27
	s_addc_u32 s2, s77, 0
	v_writelane_b32 v252, s2, 28
	s_add_u32 s2, s76, 0x8000
	v_writelane_b32 v252, s2, 29
	s_addc_u32 s2, s77, 0
	s_add_u32 s92, s76, 0x7f01e00
	s_addc_u32 s93, s77, 0
	s_add_u32 s94, s76, 0x7f01600
	s_addc_u32 s95, s77, 0
	v_writelane_b32 v252, s2, 30
	s_add_u32 s2, s76, 0x7f01400
	v_writelane_b32 v252, s2, 31
	s_addc_u32 s2, s77, 0
	s_and_b32 s69, s41, 0xffff
	v_writelane_b32 v252, s2, 32
	s_add_u32 s2, s76, 0x4000
	v_writelane_b32 v252, s2, 33
	s_addc_u32 s2, s77, 0
	v_writelane_b32 v252, s2, 34
	s_add_u32 s2, s76, 0x6860000
	s_addc_u32 s3, s77, 0
	v_writelane_b32 v252, s2, 35
	s_and_b32 s9, s81, 0xffff
	s_nop 0
	v_writelane_b32 v252, s3, 36
	s_add_u32 s2, s76, 0xd700000
	v_writelane_b32 v252, s2, 37
	s_addc_u32 s2, s77, 0
	v_writelane_b32 v252, s2, 38
	s_abs_i32 s2, s74
	v_cvt_f32_u32_e32 v1, s2
	v_writelane_b32 v252, s2, 39
	s_sub_i32 s2, 0, s2
	s_ashr_i32 s5, s4, 31
	v_rcp_iflag_f32_e32 v1, v1
	s_nop 0
	v_mul_f32_e32 v1, 0x4f7ffffe, v1
	v_cvt_u32_f32_e32 v1, v1
	s_nop 0
	v_readfirstlane_b32 s3, v1
	s_mul_i32 s2, s2, s3
	s_mul_hi_u32 s2, s3, s2
	s_add_i32 s2, s3, s2
	v_writelane_b32 v252, s2, 40
	v_writelane_b32 v252, s8, 41
	v_mov_b32_e32 v1, 0
	s_nop 0
	v_writelane_b32 v252, s9, 42
	v_writelane_b32 v252, s10, 43
	v_writelane_b32 v252, s11, 44
	s_waitcnt lgkmcnt(0)
	v_writelane_b32 v252, s0, 45
	s_mov_b32 s10, s43
	s_nop 0
	v_writelane_b32 v252, s1, 46
	s_lshl_b64 s[0:1], s[4:5], 9
	v_writelane_b32 v252, s0, 47
	s_nop 1
	v_writelane_b32 v252, s1, 48
	s_add_u32 s0, s76, 0x7f00c00
	s_addc_u32 s1, s77, 0
	v_writelane_b32 v252, s0, 49
	s_ashr_i32 s37, s36, 31
	s_add_i32 s64, 0, 0x260f8
	v_writelane_b32 v252, s1, 50
	s_lshl_b32 s0, s74, 6
	v_writelane_b32 v252, s0, 51
	s_addk_i32 s0, 0xf800
	v_writelane_b32 v252, s0, 52
	s_add_i32 s0, 0, 0x26048
	v_writelane_b32 v252, s0, 53
	s_add_i32 s0, 0, 0x2604c
	v_writelane_b32 v252, s0, 54
	s_add_i32 s0, 0, 0x26098
	v_writelane_b32 v252, s0, 55
	s_add_i32 s0, 0, 0x2609c
	v_writelane_b32 v252, s0, 56
	s_add_i32 s0, 0, 0x26090
	v_writelane_b32 v252, s0, 57
	s_add_i32 s0, 0, 0x26094
	v_writelane_b32 v252, s0, 58
	s_add_i32 s0, 0, 0x26080
	v_writelane_b32 v252, s0, 59
	s_add_i32 s0, 0, 0x26084
	v_writelane_b32 v252, s0, 60
	s_add_i32 s0, 0, 0x26128
	v_writelane_b32 v252, s0, 61
	s_add_i32 s0, 0, 0x2612c
	v_writelane_b32 v252, s0, 62
	s_add_i32 s0, 0, 0x26058
	v_writelane_b32 v252, s0, 63
	s_add_i32 s0, 0, 0x2605c
	v_writelane_b32 v253, s0, 0
	s_add_i32 s0, 0, 0x26110
	v_writelane_b32 v253, s0, 1
	s_add_i32 s0, 0, 0x26114
	v_writelane_b32 v253, s0, 2
	s_add_i32 s0, 0, 0x26068
	v_writelane_b32 v253, s0, 3
	s_add_i32 s0, 0, 0x2606c
	v_writelane_b32 v253, s0, 4
	s_add_i32 s0, 0, 0x26108
	v_writelane_b32 v253, s0, 5
	s_add_i32 s0, 0, 0x2610c
	v_writelane_b32 v253, s0, 6
	s_add_i32 s0, 0, 0x26000
	v_writelane_b32 v253, s0, 7
	s_add_i32 s0, 0, 0x26004
	v_writelane_b32 v253, s0, 8
	s_add_i32 s0, 0, 0x26070
	v_writelane_b32 v253, s0, 9
	s_add_i32 s0, 0, 0x26074
	v_writelane_b32 v253, s0, 10
	s_add_i32 s0, 0, 0x18300
	v_writelane_b32 v253, s0, 11
	s_add_i32 s0, 0, 0x1a700
	v_writelane_b32 v253, s0, 12
	s_add_i32 s0, 0, 0x1cb00
	v_writelane_b32 v253, s0, 13
	s_add_i32 s0, 0, 0x26078
	v_writelane_b32 v253, s0, 14
	s_add_i32 s0, 0, 0x2607c
	v_writelane_b32 v253, s0, 15
	s_add_i32 s0, 0, 0x26088
	v_writelane_b32 v253, s0, 16
	s_add_i32 s0, 0, 0x2608c
	v_writelane_b32 v253, s0, 17
	s_add_i32 s0, 0, 0x260a0
	v_writelane_b32 v253, s0, 18
	s_add_i32 s0, 0, 0x260a4
	v_writelane_b32 v253, s0, 19
	s_add_i32 s0, 0, 0x260a8
	v_writelane_b32 v253, s0, 20
	s_add_i32 s0, 0, 0x260ac
	v_writelane_b32 v253, s0, 21
	s_add_i32 s0, 0, 0x260b0
	v_writelane_b32 v253, s0, 22
	s_add_i32 s0, 0, 0x260b4
	v_writelane_b32 v253, s0, 23
	s_add_i32 s0, 0, 0x26100
	v_writelane_b32 v253, s0, 24
	s_add_i32 s0, 0, 0x26104
	v_writelane_b32 v253, s0, 25
	s_add_i32 s0, 0, 0x14400
	v_writelane_b32 v253, s0, 26
	s_add_i32 s0, 0, 0x26400
	v_writelane_b32 v253, s0, 27
	s_add_i32 s0, 0, 0x260b8
	v_writelane_b32 v253, s0, 28
	s_add_i32 s0, 0, 0x260bc
	v_writelane_b32 v253, s0, 29
	s_add_i32 s0, 0, 0x260c0
	v_writelane_b32 v253, s0, 30
	s_add_i32 s0, 0, 0x260c4
	v_writelane_b32 v253, s0, 31
	s_add_i32 s0, 0, 0x24880
	v_writelane_b32 v253, s0, 32
	s_add_i32 s0, 0, 0x254a0
	v_writelane_b32 v253, s0, 33
	s_add_i32 s0, 0, 0x254a8
	v_writelane_b32 v253, s0, 34
	s_add_i32 s0, 0, 0x254b0
	v_writelane_b32 v253, s0, 35
	s_add_i32 s0, 0, 0x25480
	v_writelane_b32 v253, s0, 36
	s_add_i32 s0, 0, 0x26050
	v_writelane_b32 v253, s0, 37
	s_add_i32 s0, 0, 0x26054
	v_writelane_b32 v253, s0, 38
	s_add_i32 s0, 0, 0x26060
	v_writelane_b32 v253, s0, 39
	s_add_i32 s0, 0, 0x26064
	v_writelane_b32 v253, s0, 40
	v_cmp_eq_u32_e64 s[0:1], 0, v0
	s_add_i32 s65, 0, 0x260fc
	s_nop 0
	v_writelane_b32 v253, s0, 41
	s_nop 1
	v_writelane_b32 v253, s1, 42
	s_mov_b32 s0, s4
	v_writelane_b32 v253, s0, 43
	s_nop 1
	v_writelane_b32 v253, s1, 44
	s_lshl_b64 s[0:1], s[4:5], 13
	v_writelane_b32 v253, s0, 45
	s_nop 1
	v_writelane_b32 v253, s1, 46
	s_mov_b32 s0, s36
	v_writelane_b32 v253, s0, 47
	s_nop 1
	v_writelane_b32 v253, s1, 48
	s_lshl_b64 s[0:1], s[36:37], 15
	v_writelane_b32 v253, s0, 49
	s_nop 1
	v_writelane_b32 v253, s1, 50
	v_writelane_b32 v253, s74, 51
	v_writelane_b32 v253, s76, 52
	s_nop 1
	v_writelane_b32 v253, s77, 53
	v_writelane_b32 v253, s78, 54
	s_nop 1
	v_writelane_b32 v253, s79, 55
	v_writelane_b32 v253, s80, 56
	s_nop 1
	v_writelane_b32 v253, s81, 57
	v_writelane_b32 v253, s75, 58
	v_writelane_b32 v253, s82, 59
	s_nop 1
	v_writelane_b32 v253, s83, 60
	v_writelane_b32 v253, s84, 61
	s_nop 1
	v_writelane_b32 v253, s85, 62
	v_writelane_b32 v253, s86, 63
	s_nop 1
	v_writelane_b32 v254, s87, 0
	v_writelane_b32 v254, s88, 1
	s_nop 1
	v_writelane_b32 v254, s89, 2
	v_writelane_b32 v254, s90, 3
	s_nop 1
	v_writelane_b32 v254, s91, 4
	v_writelane_b32 v254, s92, 5
	v_writelane_b32 v254, s93, 6
	v_writelane_b32 v254, s94, 7
	v_writelane_b32 v254, s95, 8
	v_writelane_b32 v254, s64, 9
	v_writelane_b32 v254, s65, 10
	s_branch .LBB0_79

;     __device__ __forceinline__ bool next(int i, Unit& u) const {
;         const int round = i / nsub; u.sub = i - round * nsub;
;         const long L = (long)round * G + c; if (L >= nwg) return false;
;         int wgid = (int)L; { const int q = nwg / NXCD, r = nwg % NXCD, xcd = wgid % NXCD, off = wgid / NXCD; wgid = (xcd < r ? xcd * (q + 1) : r * (q + 1) + (xcd - r) * q) + off; }
;         const int nig = WGM * nN, gid = wgid / nig, fm = gid * WGM, gsz = (nM - fm) < WGM ? (nM - fm) : WGM;
;         u.pm = fm + ((wgid % nig) % gsz); u.pn = (wgid % nig) / gsz;
;         u.aoff = (unsigned)u.pm * a_row + (unsigned)u.sub * a_sub; u.boff = (unsigned)u.pn * b_row + (unsigned)u.sub * b_sub;
; __global__ void __launch_bounds__(512, 2) fwd_kernel(Args args) {
;     ...
;             PHASE_BEGIN(16) {
;                 { pg8::Gemm g{proj, wb + WB_W1T, 16 * PLD, 2048, 2048, (unsigned)PLD * 2}; pg8::Sched S; S.init(16, 1, c.G, c.bid, 1, 0, 0, 0, 0); S.mode = 1;
;                   pg8::EpiCmp1 E{hidb, (const float*)(wb + WB_BH)}; pg8::gemm_phase(c.lds, c.tid, g, S, E); }
.LBB0_473:
	s_andn2_b64 vcc, exec, s[0:1]
	s_cbranch_vccnz .LBB0_553
	v_readlane_b32 s0, v251, 5
	v_mbcnt_lo_u32_b32 v0, -1, 0
	v_mbcnt_hi_u32_b32 v0, -1, v0
	v_readlane_b32 s14, v251, 0
	s_nop 0
	v_or_b32_e32 v151, s0, v0
	s_cmp_gt_i32 s14, 31
	v_readfirstlane_b32 s15, v151
	s_cbranch_scc1 .LBB0_494
	s_ashr_i32 s16, s14, 31
	s_lshr_b32 s0, s16, 29
	s_and_b32 s3, s14, 15
	s_and_b32 s0, s3, -8
	s_sub_i32 s4, s3, s0
	s_cmp_gt_i32 s4, -1
	s_mov_b64 s[0:1], -1
	s_cbranch_scc0 .LBB0_477
	s_lshl_b32 s2, s4, 1
	s_mov_b64 s[0:1], 0

; #define PG8_STAGE(bufoff, gbase, voff) do { _Pragma("unroll") for (int _i = 0; _i < 2; ++_i) \
;         __builtin_amdgcn_global_load_lds((const unsigned*)((const char*)(gbase) + (voff)[_i]), (LAS unsigned*)(lds + (bufoff) + ldsw + _i * 8192), 16, 0, 0); } while (0)
; #define PG8_WAIT_V(n) asm volatile("s_waitcnt vmcnt(" #n ")" ::: "memory")
; #define PG8_BAR __builtin_amdgcn_s_barrier()
; template <class Epi>
; __device__ __forceinline__ void gemm_phase(LAS unsigned char* lds, const int tid, const Gemm g, const Sched& S, const Epi& E) {
;     const int wid = __builtin_amdgcn_readfirstlane(tid >> 6), lane = tid & 63, wr = wid >> 2, wc = wid & 3, fr = lane & 15, fq = lane >> 4;
;     const int K = g.K, nt = K / BK;
;     unsigned voffA[2], voffB[2];
; #pragma unroll
;     for (int i = 0; i < 2; ++i) { int R, C; stage_rc(tid * 16 + i * 8192, R, C); const int Rb = Epi::PERM ? ((R & ~31) + perm32(R & 31)) : R;
;         voffA[i] = (unsigned)(R * g.lda + C) * 2u; voffB[i] = (unsigned)(Rb * g.ldb + C) * 2u; }
;     const size_t kstep = (size_t)(BK * 2), kstA = g.kstepA;
;     const size_t hstepA = (size_t)HALF * g.lda * 2, hstepB = (size_t)HALF * g.ldb * 2;
;     const unsigned ldsw = (unsigned)wid * 1024u;
;     const int aoff = lds_byte(wr * 64 + fr, fq * 8), boff = lds_byte(wc * 32 + fr, fq * 8);
;     ...
;     Unit cur, nxt; int ui = 0;
;     if (!S.next(0, cur)) return;
;     f32x4 acc[2][2][4][2];
; #pragma unroll
;     for (int a = 0; a < 2; ++a)
; #pragma unroll
;         for (int b = 0; b < 2; ++b)
; #pragma unroll
;             for (int m = 0; m < 4; ++m)
; #pragma unroll
;                 for (int n = 0; n < 2; ++n) acc[a][b][m][n] = (f32x4){0.f, 0.f, 0.f, 0.f};
;     bf16x8 At[4][2], B0[2][2], B1[2][2];
;     const char* cA = (const char*)g.A + cur.aoff; const char* cB = (const char*)g.Bt + cur.boff;
;     PG8_STAGE(PG8_SB(0, 0), cB, voffB); PG8_STAGE(PG8_SA(0, 0), cA, voffA); PG8_STAGE(PG8_SB(0, 1), cB + hstepB, voffB); PG8_STAGE(PG8_SA(0, 1), cA + hstepA, voffA);
;     if (wr == 1) PG8_BAR;
;     PG8_WAIT_V(4); PG8_BAR;
;     PG8_STAGE(PG8_SB(1, 0), cB + kstep, voffB); PG8_STAGE(PG8_SA(1, 0), cA + kstA, voffA); PG8_STAGE(PG8_SB(1, 1), cB + hstepB + kstep, voffB);
;     PG8_WAIT_V(6); PG8_BAR;
.LBB0_479:
	v_ashrrev_i32_e32 v2, 31, v151
	v_lshrrev_b32_e32 v2, 26, v2
	v_add_u32_e32 v2, v151, v2
	v_ashrrev_i32_e32 v6, 6, v2
	v_bfe_i32 v2, v151, 27, 1
	v_lshlrev_b32_e32 v0, 4, v151
	v_lshrrev_b32_e32 v2, 22, v2
	v_add_u32_e32 v2, v0, v2
	v_and_b32_e32 v2, 0xfffffc00, v2
	v_sub_u32_e32 v2, v0, v2
	v_lshrrev_b32_e32 v3, 4, v2
	v_bitop3_b32 v2, v3, v2, 32 bitop3:0x6c
	v_ashrrev_i32_e32 v4, 31, v2
	v_lshrrev_b32_e32 v4, 26, v4
	v_add_u32_e32 v4, v2, v4
	v_lshlrev_b32_e32 v3, 3, v6
	v_ashrrev_i32_e32 v7, 6, v4
	v_and_b32_e32 v4, 0xc0, v4
	v_and_b32_e32 v3, -16, v3
	v_sub_u32_e32 v2, v2, v4
	v_mov_b32_e32 v11, 1
	v_add_u32_e32 v3, v7, v3
	v_ashrrev_i16_sdwa v2, v11, sext(v2) dst_sel:DWORD dst_unused:UNUSED_PAD src0_sel:DWORD src1_sel:BYTE_0
	v_lshlrev_b32_e32 v5, 5, v6
	v_bfe_i32 v8, v2, 0, 16
	v_lshlrev_b32_e32 v2, 1, v3
	v_lshrrev_b32_e32 v4, 2, v3
	v_and_b32_e32 v9, 3, v7
	s_mov_b32 s1, 0xfffe0
	v_and_b32_e32 v5, 32, v5
	v_and_b32_e32 v2, 24, v2
	v_and_b32_e32 v4, 4, v4
	v_and_or_b32 v9, v3, s1, v9
	v_or3_b32 v2, v9, v4, v2
	v_add_lshl_u32 v4, v5, v8, 1
	v_add_u32_e32 v0, 0x2000, v0
	v_lshl_add_u32 v144, v2, 12, v4
	v_ashrrev_i32_e32 v2, 31, v0
	v_lshrrev_b32_e32 v2, 22, v2
	v_add_u32_e32 v2, v0, v2
	v_ashrrev_i32_e32 v9, 10, v2
	v_mul_i32_i24_e32 v2, 0x400, v9
	v_sub_u32_e32 v0, v0, v2
	v_lshrrev_b32_e32 v2, 4, v0
	v_bitop3_b32 v0, v2, v0, 32 bitop3:0x6c
	s_add_i32 s22, s2, s3
	v_lshl_add_u32 v142, v3, 17, v4
	v_ashrrev_i32_e32 v3, 31, v0
	s_ashr_i32 s2, s22, 31
	v_lshrrev_b32_e32 v3, 26, v3
	s_lshr_b32 s2, s2, 29
	v_lshlrev_b32_e32 v2, 3, v9
	v_add_u32_e32 v3, v0, v3
	s_add_i32 s2, s22, s2
	v_and_b32_e32 v2, -16, v2
	v_ashrrev_i32_e32 v10, 6, v3
	s_and_b32 s2, s2, -8
	v_add_u32_e32 v2, v10, v2
	v_and_b32_e32 v5, 3, v10
	s_sub_i32 s2, s22, s2
	v_and_or_b32 v5, v2, s1, v5
	s_ashr_i32 s1, s15, 6
	s_lshl_b32 s3, s2, 25
	s_ashr_i32 s0, s15, 8
	s_lshl_b32 s17, s1, 10
	s_and_b32 s3, s3, 0x6000000
	s_cmp_lt_u32 s22, 8
	s_movk_i32 s4, 0x1200
	s_cselect_b32 s4, s4, 0x1300
	s_lshl_b32 s2, s2, 5
	s_and_b32 s2, s2, 0x80
	v_and_b32_e32 v3, 0xc0, v3
	s_or_b32 s2, s2, s3
	s_lshl_b32 s3, s22, 17
	v_sub_u32_e32 v0, v0, v3
	s_or_b32 s2, s2, s4
	s_and_b32 s3, s3, 0xfff00000
	v_readlane_b32 s4, v251, 10
	v_ashrrev_i16_sdwa v0, v11, sext(v0) dst_sel:DWORD dst_unused:UNUSED_PAD src0_sel:DWORD src1_sel:BYTE_0
	s_add_u32 s6, s4, s3
	v_readlane_b32 s3, v251, 11
	v_lshlrev_b32_e32 v4, 5, v9
	v_bfe_i32 v11, v0, 0, 16
	v_lshlrev_b32_e32 v0, 1, v2
	v_lshrrev_b32_e32 v3, 2, v2
	s_addc_u32 s7, s3, 0
	s_lshr_b32 s3, s14, 4
	s_lshl_b32 s3, s3, 11
	s_add_u32 s6, s6, s3
	s_addc_u32 s7, s7, 0
	s_add_i32 s20, s17, 0
	v_and_b32_e32 v4, 32, v4
	v_and_b32_e32 v0, 24, v0
	v_and_b32_e32 v3, 4, v3
	s_add_i32 m0, s20, 0x10000
	v_or3_b32 v0, v5, v3, v0
	v_add_lshl_u32 v3, v4, v11, 1
	global_load_lds_dwordx4 v144, s[6:7]
	s_add_i32 m0, s20, 0x12000
	v_lshl_add_u32 v148, v0, 12, v3
	s_add_u32 s8, s80, s2
	global_load_lds_dwordx4 v148, s[6:7]
	s_addc_u32 s9, s81, 0
	s_lshr_b32 s3, s14, 4
	s_lshl_b32 s3, s3, 17
	s_add_u32 s8, s8, s3
	s_addc_u32 s9, s9, 0
	s_mov_b32 m0, s20
	s_add_i32 s21, s20, 0x2000
	v_lshl_add_u32 v146, v2, 17, v3
	global_load_lds_dwordx4 v142, s[8:9]
	s_mov_b32 m0, s21
	s_add_u32 s2, s6, 0x80000
	global_load_lds_dwordx4 v146, s[8:9]
	s_addc_u32 s3, s7, 0
	s_add_i32 m0, s20, 0x14000
	v_mov_b32_e32 v145, v1
	global_load_lds_dwordx4 v144, s[2:3]
	s_add_i32 m0, s20, 0x16000
	v_mov_b32_e32 v149, v1
	global_load_lds_dwordx4 v148, s[2:3]
	s_add_u32 s2, s8, 0x1000000
	s_addc_u32 s3, s9, 0
	s_add_i32 s26, s20, 0x4000
	s_mov_b32 m0, s26
	s_add_i32 s27, s20, 0x6000
	global_load_lds_dwordx4 v142, s[2:3]
	s_mov_b32 m0, s27
	v_lshl_add_u64 v[2:3], s[6:7], 0, v[144:145]
	global_load_lds_dwordx4 v146, s[2:3]
	s_cmp_lg_u32 s0, 1
	v_lshl_add_u64 v[4:5], s[6:7], 0, v[148:149]
	s_cbranch_scc1 .LBB0_481
	s_barrier

; #define PG8_STAGE(bufoff, gbase, voff) do { _Pragma("unroll") for (int _i = 0; _i < 2; ++_i) \
;         __builtin_amdgcn_global_load_lds((const unsigned*)((const char*)(gbase) + (voff)[_i]), (LAS unsigned*)(lds + (bufoff) + ldsw + _i * 8192), 16, 0, 0); } while (0)
; #define PG8_LDA(dst, b, h) do { _Pragma("unroll") for (int m = 0; m < 4; ++m) _Pragma("unroll") for (int k = 0; k < 2; ++k) dst[m][k] = *(const LAS bf16x8*)(lds + PG8_SA(b, h) + aoff + m * 2048 + k * 1024); } while (0)
; #define PG8_WAIT_V(n) asm volatile("s_waitcnt vmcnt(" #n ")" ::: "memory")
; template <class Epi>
; __device__ __forceinline__ void gemm_phase(LAS unsigned char* lds, const int tid, const Gemm g, const Sched& S, const Epi& E) {
;     ...
;     Unit cur, nxt; int ui = 0;
;     if (!S.next(0, cur)) return;
;     f32x4 acc[2][2][4][2];
; #pragma unroll
;     for (int a = 0; a < 2; ++a)
; #pragma unroll
;         for (int b = 0; b < 2; ++b)
; #pragma unroll
;             for (int m = 0; m < 4; ++m)
; #pragma unroll
;                 for (int n = 0; n < 2; ++n) acc[a][b][m][n] = (f32x4){0.f, 0.f, 0.f, 0.f};
;     bf16x8 At[4][2], B0[2][2], B1[2][2];
;     const char* cA = (const char*)g.A + cur.aoff; const char* cB = (const char*)g.Bt + cur.boff;
;     PG8_STAGE(PG8_SB(0, 0), cB, voffB); PG8_STAGE(PG8_SA(0, 0), cA, voffA); PG8_STAGE(PG8_SB(0, 1), cB + hstepB, voffB); PG8_STAGE(PG8_SA(0, 1), cA + hstepA, voffA);
;     if (wr == 1) PG8_BAR;
;     PG8_WAIT_V(4); PG8_BAR;
;     PG8_STAGE(PG8_SB(1, 0), cB + kstep, voffB); PG8_STAGE(PG8_SA(1, 0), cA + kstA, voffA); PG8_STAGE(PG8_SB(1, 1), cB + hstepB + kstep, voffB);
;     PG8_WAIT_V(6); PG8_BAR;
;     for (;;) {
;         const bool has_next = S.next(ui + 1, nxt);
;         const char* nA = has_next ? (const char*)g.A + nxt.aoff : cA; const char* nB = has_next ? (const char*)g.Bt + nxt.boff : cB;
;         for (int t = 0; t < nt; t += 2) {
;             const bool last = (t == nt - 2);
;             const char* a1 = cA + (size_t)(t + 1) * kstA;
;             const char* a2 = last ? nA : cA + (size_t)(t + 2) * kstA; const char* b2 = last ? nB : cB + (size_t)(t + 2) * kstep;
;             const char* a3 = a2 + kstA; const char* b3 = b2 + kstep;
;             PG8_LDB(B0, 0, 0); PG8_SCHED; PG8_LDA(At, 0, 0); PG8_STAGE(PG8_SA(1, 1), a1 + hstepA, voffA);
;             PG8_WAIT_L(8); PG8_BAR; PG8_WAIT_L(0); PG8_MMA(0, 0, At, B0); PG8_BAR; PG8_SCHED;
.LBB0_488:
	v_cmp_lt_i64_e64 s[10:11], s[2:3], 16
	s_add_u32 s2, s80, s38
	s_addc_u32 s3, s81, 0
	s_and_b64 s[4:5], s[10:11], exec
	v_readlane_b32 s4, v251, 10
	s_cselect_b32 s42, s3, s9
	s_cselect_b32 s46, s2, s8
	s_add_u32 s4, s4, s39
	v_readlane_b32 s5, v251, 11
	s_addc_u32 s5, s5, 0
	s_and_b64 s[10:11], s[10:11], exec
	s_cselect_b32 s47, s5, s7
	s_cselect_b32 s48, s4, s6
	s_add_u32 s49, s6, 0x100
	s_addc_u32 s50, s7, 0
	s_add_u32 s6, s8, 0x1002000
	v_mov_b32_e32 v2, 0
	s_addc_u32 s7, s9, 0
	s_mov_b32 s51, 14
	v_mov_b32_e32 v3, v2
	v_mov_b32_e32 v4, v2
	v_mov_b32_e32 v5, v2
	v_mov_b32_e32 v6, v2
	v_mov_b32_e32 v7, v2
	v_mov_b32_e32 v8, v2
	v_mov_b32_e32 v9, v2
	v_mov_b32_e32 v18, v2
	v_mov_b32_e32 v19, v2
	v_mov_b32_e32 v20, v2
	v_mov_b32_e32 v21, v2
	v_mov_b32_e32 v22, v2
	v_mov_b32_e32 v23, v2
	v_mov_b32_e32 v24, v2
	v_mov_b32_e32 v25, v2
	v_mov_b32_e32 v34, v2
	v_mov_b32_e32 v35, v2
	v_mov_b32_e32 v36, v2
	v_mov_b32_e32 v37, v2
	v_mov_b32_e32 v42, v2
	v_mov_b32_e32 v43, v2
	v_mov_b32_e32 v44, v2
	v_mov_b32_e32 v45, v2
	v_mov_b32_e32 v62, v2
	v_mov_b32_e32 v63, v2
	v_mov_b32_e32 v64, v2
	v_mov_b32_e32 v65, v2
	v_mov_b32_e32 v70, v2
	v_mov_b32_e32 v71, v2
	v_mov_b32_e32 v72, v2
	v_mov_b32_e32 v73, v2
	v_mov_b32_e32 v10, v2
	v_mov_b32_e32 v11, v2
	v_mov_b32_e32 v12, v2
	v_mov_b32_e32 v13, v2
	v_mov_b32_e32 v14, v2
	v_mov_b32_e32 v15, v2
	v_mov_b32_e32 v16, v2
	v_mov_b32_e32 v17, v2
	v_mov_b32_e32 v26, v2
	v_mov_b32_e32 v27, v2
	v_mov_b32_e32 v28, v2
	v_mov_b32_e32 v29, v2
	v_mov_b32_e32 v30, v2
	v_mov_b32_e32 v31, v2
	v_mov_b32_e32 v32, v2
	v_mov_b32_e32 v33, v2
	v_mov_b32_e32 v50, v2
	v_mov_b32_e32 v51, v2
	v_mov_b32_e32 v52, v2
	v_mov_b32_e32 v53, v2
	v_mov_b32_e32 v58, v2
	v_mov_b32_e32 v59, v2
	v_mov_b32_e32 v60, v2
	v_mov_b32_e32 v61, v2
	v_mov_b32_e32 v74, v2
	v_mov_b32_e32 v75, v2
	v_mov_b32_e32 v76, v2
	v_mov_b32_e32 v77, v2
	v_mov_b32_e32 v78, v2
	v_mov_b32_e32 v79, v2
	v_mov_b32_e32 v80, v2
	v_mov_b32_e32 v81, v2
	v_mov_b32_e32 v82, v2
	v_mov_b32_e32 v83, v2
	v_mov_b32_e32 v84, v2
	v_mov_b32_e32 v85, v2
	v_mov_b32_e32 v86, v2
	v_mov_b32_e32 v87, v2
	v_mov_b32_e32 v88, v2
	v_mov_b32_e32 v89, v2
	v_mov_b32_e32 v98, v2
	v_mov_b32_e32 v99, v2
	v_mov_b32_e32 v100, v2
	v_mov_b32_e32 v101, v2
	v_mov_b32_e32 v102, v2
	v_mov_b32_e32 v103, v2
	v_mov_b32_e32 v104, v2
	v_mov_b32_e32 v105, v2
	v_mov_b32_e32 v114, v2
	v_mov_b32_e32 v115, v2
	v_mov_b32_e32 v116, v2
	v_mov_b32_e32 v117, v2
	v_mov_b32_e32 v118, v2
	v_mov_b32_e32 v119, v2
	v_mov_b32_e32 v120, v2
	v_mov_b32_e32 v121, v2
	v_mov_b32_e32 v130, v2
	v_mov_b32_e32 v131, v2
	v_mov_b32_e32 v132, v2
	v_mov_b32_e32 v133, v2
	v_mov_b32_e32 v134, v2
	v_mov_b32_e32 v135, v2
	v_mov_b32_e32 v136, v2
	v_mov_b32_e32 v137, v2
	v_mov_b32_e32 v90, v2
	v_mov_b32_e32 v91, v2
	v_mov_b32_e32 v92, v2
	v_mov_b32_e32 v93, v2
	v_mov_b32_e32 v94, v2
	v_mov_b32_e32 v95, v2
	v_mov_b32_e32 v96, v2
	v_mov_b32_e32 v97, v2
	v_mov_b32_e32 v106, v2
	v_mov_b32_e32 v107, v2
	v_mov_b32_e32 v108, v2
	v_mov_b32_e32 v109, v2
	v_mov_b32_e32 v110, v2
	v_mov_b32_e32 v111, v2
	v_mov_b32_e32 v112, v2
	v_mov_b32_e32 v113, v2
	v_mov_b32_e32 v122, v2
	v_mov_b32_e32 v123, v2
	v_mov_b32_e32 v124, v2
	v_mov_b32_e32 v125, v2
	v_mov_b32_e32 v126, v2
	v_mov_b32_e32 v127, v2
	v_mov_b32_e32 v128, v2
	v_mov_b32_e32 v129, v2
	v_mov_b32_e32 v38, v2
	v_mov_b32_e32 v39, v2
	v_mov_b32_e32 v40, v2
	v_mov_b32_e32 v41, v2
	v_mov_b32_e32 v66, v2
	v_mov_b32_e32 v67, v2
	v_mov_b32_e32 v68, v2
	v_mov_b32_e32 v69, v2
.LBB0_489:
	s_add_u32 s8, s6, 0xff002000
	s_addc_u32 s9, s7, -1
	s_cmp_eq_u32 s51, 28
	s_cselect_b32 s12, s46, s8
	s_cselect_b32 s13, s42, s9
	s_cselect_b32 s8, s48, s49
	s_cselect_b32 s9, s47, s50
	s_add_u32 s10, s12, 0x2000
	s_addc_u32 s11, s13, 0
	s_add_i32 s52, 0, 0x10000
	v_add_u32_e32 v0, s52, v165
	ds_read_b128 v[46:49], v0
	ds_read_b128 v[54:57], v0 offset:1024
	ds_read_b128 v[138:141], v0 offset:2048
	ds_read_b128 v[158:161], v0 offset:3072
	v_lshl_add_u64 v[162:163], s[6:7], 0, v[154:155]
	s_add_i32 m0, s20, 0xc000
	ds_read_b128 v[168:171], v166
	ds_read_b128 v[172:175], v166 offset:1024
	ds_read_b128 v[176:179], v166 offset:2048
	ds_read_b128 v[180:183], v166 offset:3072
	ds_read_b128 v[196:199], v166 offset:4096
	ds_read_b128 v[200:203], v166 offset:5120
	ds_read_b128 v[204:207], v166 offset:6144
	ds_read_b128 v[208:211], v166 offset:7168
	global_load_lds_dwordx4 v[162:163], off
	v_lshl_add_u64 v[162:163], s[6:7], 0, v[156:157]
	s_add_i32 m0, s20, 0xe000
	s_nop 0
	global_load_lds_dwordx4 v[162:163], off
	s_waitcnt lgkmcnt(8)
	s_barrier
	s_waitcnt lgkmcnt(0)
	s_setprio 1
	s_waitcnt lgkmcnt(0)
	v_mfma_f32_16x16x32_bf16 v[66:69], v[46:49], v[168:171], v[66:69]
	v_mfma_f32_16x16x32_bf16 v[38:41], v[138:141], v[168:171], v[38:41]
	v_mfma_f32_16x16x32_bf16 v[126:129], v[46:49], v[176:179], v[126:129]
	v_mfma_f32_16x16x32_bf16 v[122:125], v[138:141], v[176:179], v[122:125]
	v_mfma_f32_16x16x32_bf16 v[110:113], v[46:49], v[196:199], v[110:113]
	v_mfma_f32_16x16x32_bf16 v[106:109], v[138:141], v[196:199], v[106:109]
	v_mfma_f32_16x16x32_bf16 v[94:97], v[46:49], v[204:207], v[94:97]
	v_mfma_f32_16x16x32_bf16 v[90:93], v[138:141], v[204:207], v[90:93]
	v_mfma_f32_16x16x32_bf16 v[66:69], v[54:57], v[172:175], v[66:69]
	v_mfma_f32_16x16x32_bf16 v[38:41], v[158:161], v[172:175], v[38:41]
	v_mfma_f32_16x16x32_bf16 v[126:129], v[54:57], v[180:183], v[126:129]
	v_mfma_f32_16x16x32_bf16 v[122:125], v[158:161], v[180:183], v[122:125]
	v_mfma_f32_16x16x32_bf16 v[110:113], v[54:57], v[200:203], v[110:113]
	v_mfma_f32_16x16x32_bf16 v[106:109], v[158:161], v[200:203], v[106:109]
	v_mfma_f32_16x16x32_bf16 v[94:97], v[54:57], v[208:211], v[94:97]
	v_mfma_f32_16x16x32_bf16 v[90:93], v[158:161], v[208:211], v[90:93]
	s_setprio 0
	s_barrier
; #define PG8_STAGE(bufoff, gbase, voff) do { _Pragma("unroll") for (int _i = 0; _i < 2; ++_i) \
;         __builtin_amdgcn_global_load_lds((const unsigned*)((const char*)(gbase) + (voff)[_i]), (LAS unsigned*)(lds + (bufoff) + ldsw + _i * 8192), 16, 0, 0); } while (0)
; #define PG8_LDA(dst, b, h) do { _Pragma("unroll") for (int m = 0; m < 4; ++m) _Pragma("unroll") for (int k = 0; k < 2; ++k) dst[m][k] = *(const LAS bf16x8*)(lds + PG8_SA(b, h) + aoff + m * 2048 + k * 1024); } while (0)
; #define PG8_LDB(dst, b, h) do { _Pragma("unroll") for (int n = 0; n < 2; ++n) _Pragma("unroll") for (int k = 0; k < 2; ++k) dst[n][k] = *(const LAS bf16x8*)(lds + PG8_SB(b, h) + boff + n * 2048 + k * 1024); } while (0)
; #define PG8_MMA(ai, bj, At, Bt) do { __builtin_amdgcn_s_setprio(1); _Pragma("unroll") for (int m = 0; m < 4; ++m) _Pragma("unroll") for (int n = 0; n < 2; ++n) _Pragma("unroll") for (int k = 0; k < 2; ++k) \
;         acc[ai][bj][m][n] = __builtin_amdgcn_mfma_f32_16x16x32_bf16(Bt[n][k], At[m][k], acc[ai][bj][m][n], 0, 0, 0); __builtin_amdgcn_s_setprio(0); } while (0)
; #define PG8_WAIT_V(n) asm volatile("s_waitcnt vmcnt(" #n ")" ::: "memory")
; #define PG8_WAIT_L(n) asm volatile("s_waitcnt lgkmcnt(" #n ")" ::: "memory")
; #define PG8_BAR __builtin_amdgcn_s_barrier()
; #define PG8_SCHED __builtin_amdgcn_sched_barrier(0)
; template <class Epi>
; __device__ __forceinline__ void gemm_phase(LAS unsigned char* lds, const int tid, const Gemm g, const Sched& S, const Epi& E) {
;     ...
;             PG8_LDB(B1, 0, 1); PG8_STAGE(PG8_SB(0, 0), b2, voffB);
;             PG8_BAR; PG8_WAIT_L(0); PG8_MMA(0, 1, At, B1); PG8_BAR;
;             PG8_LDA(At, 0, 1); PG8_STAGE(PG8_SA(0, 0), a2, voffA);
;             PG8_BAR; PG8_WAIT_L(0); PG8_MMA(1, 0, At, B0); PG8_BAR; PG8_SCHED;
;             PG8_STAGE(PG8_SB(0, 1), b2 + hstepB, voffB);
;             PG8_WAIT_V(6); PG8_BAR; PG8_MMA(1, 1, At, B1); PG8_BAR;
;             PG8_LDB(B0, 1, 0); PG8_SCHED; PG8_LDA(At, 1, 0); PG8_STAGE(PG8_SA(0, 1), a2 + hstepA, voffA);
	s_add_i32 s54, 0, 0x14000
	s_add_i32 s52, s52, s17
	v_add_u32_e32 v0, s54, v165
	v_lshl_add_u64 v[162:163], s[8:9], 0, v[144:145]
	s_mov_b32 m0, s52
	ds_read_b128 v[212:215], v0
	ds_read_b128 v[216:219], v0 offset:1024
	ds_read_b128 v[220:223], v0 offset:2048
	ds_read_b128 v[224:227], v0 offset:3072
	global_load_lds_dwordx4 v[162:163], off
	v_lshl_add_u64 v[184:185], s[8:9], 0, v[148:149]
	s_add_i32 m0, s52, 0x2000
	s_nop 0
	global_load_lds_dwordx4 v[184:185], off
	s_barrier
	s_waitcnt lgkmcnt(0)
	s_setprio 1
	s_waitcnt lgkmcnt(0)
	v_mfma_f32_16x16x32_bf16 v[134:137], v[212:215], v[168:171], v[134:137]
	v_mfma_f32_16x16x32_bf16 v[130:133], v[220:223], v[168:171], v[130:133]
	v_mfma_f32_16x16x32_bf16 v[118:121], v[212:215], v[176:179], v[118:121]
	v_mfma_f32_16x16x32_bf16 v[114:117], v[220:223], v[176:179], v[114:117]
	v_mfma_f32_16x16x32_bf16 v[102:105], v[212:215], v[196:199], v[102:105]
	v_mfma_f32_16x16x32_bf16 v[98:101], v[220:223], v[196:199], v[98:101]
	v_mfma_f32_16x16x32_bf16 v[86:89], v[212:215], v[204:207], v[86:89]
	v_mfma_f32_16x16x32_bf16 v[82:85], v[220:223], v[204:207], v[82:85]
	v_mfma_f32_16x16x32_bf16 v[134:137], v[216:219], v[172:175], v[134:137]
	v_mfma_f32_16x16x32_bf16 v[130:133], v[224:227], v[172:175], v[130:133]
	v_mfma_f32_16x16x32_bf16 v[118:121], v[216:219], v[180:183], v[118:121]
	v_mfma_f32_16x16x32_bf16 v[114:117], v[224:227], v[180:183], v[114:117]
	v_mfma_f32_16x16x32_bf16 v[102:105], v[216:219], v[200:203], v[102:105]
	v_mfma_f32_16x16x32_bf16 v[98:101], v[224:227], v[200:203], v[98:101]
	v_mfma_f32_16x16x32_bf16 v[86:89], v[216:219], v[208:211], v[86:89]
	v_mfma_f32_16x16x32_bf16 v[82:85], v[224:227], v[208:211], v[82:85]
	s_setprio 0
	s_mov_b32 m0, s20
	v_lshl_add_u64 v[228:229], s[12:13], 0, v[142:143]
	s_barrier
	ds_read_b128 v[168:171], v166 offset:16384
	ds_read_b128 v[172:175], v166 offset:17408
	ds_read_b128 v[176:179], v166 offset:18432
	ds_read_b128 v[180:183], v166 offset:19456
	ds_read_b128 v[196:199], v166 offset:20480
	ds_read_b128 v[200:203], v166 offset:21504
	ds_read_b128 v[204:207], v166 offset:22528
	ds_read_b128 v[208:211], v166 offset:23552
	global_load_lds_dwordx4 v[228:229], off
	v_lshl_add_u64 v[228:229], s[12:13], 0, v[146:147]
	s_mov_b32 m0, s21
	s_nop 0
	global_load_lds_dwordx4 v[228:229], off
	s_barrier
	s_waitcnt lgkmcnt(0)
	s_setprio 1
	s_waitcnt lgkmcnt(0)
	v_mfma_f32_16x16x32_bf16 v[78:81], v[46:49], v[168:171], v[78:81]
	v_mfma_f32_16x16x32_bf16 v[74:77], v[138:141], v[168:171], v[74:77]
	v_mfma_f32_16x16x32_bf16 v[58:61], v[46:49], v[176:179], v[58:61]
	v_mfma_f32_16x16x32_bf16 v[50:53], v[138:141], v[176:179], v[50:53]
	v_mfma_f32_16x16x32_bf16 v[30:33], v[46:49], v[196:199], v[30:33]
	v_mfma_f32_16x16x32_bf16 v[26:29], v[138:141], v[196:199], v[26:29]
	v_mfma_f32_16x16x32_bf16 v[14:17], v[46:49], v[204:207], v[14:17]
	v_mfma_f32_16x16x32_bf16 v[10:13], v[138:141], v[204:207], v[10:13]
	v_mfma_f32_16x16x32_bf16 v[78:81], v[54:57], v[172:175], v[78:81]
	v_mfma_f32_16x16x32_bf16 v[74:77], v[158:161], v[172:175], v[74:77]
	v_mfma_f32_16x16x32_bf16 v[58:61], v[54:57], v[180:183], v[58:61]
	v_mfma_f32_16x16x32_bf16 v[50:53], v[158:161], v[180:183], v[50:53]
	v_mfma_f32_16x16x32_bf16 v[30:33], v[54:57], v[200:203], v[30:33]
	v_mfma_f32_16x16x32_bf16 v[26:29], v[158:161], v[200:203], v[26:29]
	v_mfma_f32_16x16x32_bf16 v[14:17], v[54:57], v[208:211], v[14:17]
	v_mfma_f32_16x16x32_bf16 v[10:13], v[158:161], v[208:211], v[10:13]
	s_setprio 0
	s_barrier
	s_add_u32 s52, s8, 0x80000
	s_addc_u32 s53, s9, 0
	s_add_i32 s54, s54, s17
	v_lshl_add_u64 v[46:47], s[52:53], 0, v[144:145]
	s_mov_b32 m0, s54
	s_nop 0
	global_load_lds_dwordx4 v[46:47], off
	v_lshl_add_u64 v[46:47], s[52:53], 0, v[148:149]
	s_add_i32 m0, s54, 0x2000
	s_nop 0
	global_load_lds_dwordx4 v[46:47], off
	s_waitcnt vmcnt(6)
	s_barrier
	s_setprio 1
	v_mfma_f32_16x16x32_bf16 v[42:45], v[212:215], v[176:179], v[42:45]
	v_mfma_f32_16x16x32_bf16 v[34:37], v[220:223], v[176:179], v[34:37]
	v_mfma_f32_16x16x32_bf16 v[22:25], v[212:215], v[196:199], v[22:25]
	v_mfma_f32_16x16x32_bf16 v[18:21], v[220:223], v[196:199], v[18:21]
	v_mfma_f32_16x16x32_bf16 v[6:9], v[212:215], v[204:207], v[6:9]
	v_mfma_f32_16x16x32_bf16 v[2:5], v[220:223], v[204:207], v[2:5]
	v_mfma_f32_16x16x32_bf16 v[46:49], v[212:215], v[168:171], v[70:73]
	v_mfma_f32_16x16x32_bf16 v[54:57], v[220:223], v[168:171], v[62:65]
	v_mfma_f32_16x16x32_bf16 v[42:45], v[216:219], v[180:183], v[42:45]
	v_mfma_f32_16x16x32_bf16 v[34:37], v[224:227], v[180:183], v[34:37]
	v_mfma_f32_16x16x32_bf16 v[22:25], v[216:219], v[200:203], v[22:25]
	v_mfma_f32_16x16x32_bf16 v[18:21], v[224:227], v[200:203], v[18:21]
	v_mfma_f32_16x16x32_bf16 v[6:9], v[216:219], v[208:211], v[6:9]
	v_mfma_f32_16x16x32_bf16 v[2:5], v[224:227], v[208:211], v[2:5]
	v_mfma_f32_16x16x32_bf16 v[46:49], v[216:219], v[172:175], v[46:49]
	v_mfma_f32_16x16x32_bf16 v[54:57], v[224:227], v[172:175], v[54:57]
	s_setprio 0
	s_add_i32 s52, 0, 0x18000
	v_add_u32_e32 v0, s52, v165
	s_barrier
	ds_read_b128 v[62:65], v0
	ds_read_b128 v[70:73], v0 offset:1024
	ds_read_b128 v[138:141], v0 offset:2048
	ds_read_b128 v[158:161], v0 offset:3072
	s_add_u32 s12, s12, 0x1000000
	s_addc_u32 s13, s13, 0
	s_mov_b32 m0, s26
	v_lshl_add_u64 v[212:213], s[12:13], 0, v[142:143]
	ds_read_b128 v[168:171], v166 offset:32768
	ds_read_b128 v[172:175], v166 offset:33792
	ds_read_b128 v[176:179], v166 offset:34816
	ds_read_b128 v[180:183], v166 offset:35840
	ds_read_b128 v[196:199], v166 offset:36864
	ds_read_b128 v[200:203], v166 offset:37888
	ds_read_b128 v[204:207], v166 offset:38912
	ds_read_b128 v[208:211], v166 offset:39936
	global_load_lds_dwordx4 v[212:213], off
	v_lshl_add_u64 v[212:213], s[12:13], 0, v[146:147]
	s_mov_b32 m0, s27
	s_nop 0
	global_load_lds_dwordx4 v[212:213], off
	s_waitcnt lgkmcnt(8)
	s_barrier
; #define PG8_STAGE(bufoff, gbase, voff) do { _Pragma("unroll") for (int _i = 0; _i < 2; ++_i) \
;         __builtin_amdgcn_global_load_lds((const unsigned*)((const char*)(gbase) + (voff)[_i]), (LAS unsigned*)(lds + (bufoff) + ldsw + _i * 8192), 16, 0, 0); } while (0)
; #define PG8_LDA(dst, b, h) do { _Pragma("unroll") for (int m = 0; m < 4; ++m) _Pragma("unroll") for (int k = 0; k < 2; ++k) dst[m][k] = *(const LAS bf16x8*)(lds + PG8_SA(b, h) + aoff + m * 2048 + k * 1024); } while (0)
; #define PG8_LDB(dst, b, h) do { _Pragma("unroll") for (int n = 0; n < 2; ++n) _Pragma("unroll") for (int k = 0; k < 2; ++k) dst[n][k] = *(const LAS bf16x8*)(lds + PG8_SB(b, h) + boff + n * 2048 + k * 1024); } while (0)
; #define PG8_MMA(ai, bj, At, Bt) do { __builtin_amdgcn_s_setprio(1); _Pragma("unroll") for (int m = 0; m < 4; ++m) _Pragma("unroll") for (int n = 0; n < 2; ++n) _Pragma("unroll") for (int k = 0; k < 2; ++k) \
;         acc[ai][bj][m][n] = __builtin_amdgcn_mfma_f32_16x16x32_bf16(Bt[n][k], At[m][k], acc[ai][bj][m][n], 0, 0, 0); __builtin_amdgcn_s_setprio(0); } while (0)
; #define PG8_WAIT_L(n) asm volatile("s_waitcnt lgkmcnt(" #n ")" ::: "memory")
; #define PG8_BAR __builtin_amdgcn_s_barrier()
; #define PG8_SCHED __builtin_amdgcn_sched_barrier(0)
; template <class Epi>
; __device__ __forceinline__ void gemm_phase(LAS unsigned char* lds, const int tid, const Gemm g, const Sched& S, const Epi& E) {
;     ...
;             PG8_WAIT_L(8); PG8_BAR; PG8_WAIT_L(0); PG8_MMA(0, 0, At, B0); PG8_BAR; PG8_SCHED;
;             PG8_LDB(B1, 1, 1); PG8_STAGE(PG8_SB(1, 0), b3, voffB);
;             PG8_BAR; PG8_WAIT_L(0); PG8_MMA(0, 1, At, B1); PG8_BAR;
;             PG8_LDA(At, 1, 1); PG8_STAGE(PG8_SA(1, 0), a3, voffA);
;             PG8_BAR; PG8_WAIT_L(0); PG8_MMA(1, 0, At, B0); PG8_BAR; PG8_SCHED;
;             PG8_STAGE(PG8_SB(1, 1), b3 + hstepB, voffB);
	s_waitcnt lgkmcnt(0)
	s_setprio 1
	s_waitcnt lgkmcnt(0)
	v_mfma_f32_16x16x32_bf16 v[66:69], v[62:65], v[168:171], v[66:69]
	v_mfma_f32_16x16x32_bf16 v[38:41], v[138:141], v[168:171], v[38:41]
	v_mfma_f32_16x16x32_bf16 v[126:129], v[62:65], v[176:179], v[126:129]
	v_mfma_f32_16x16x32_bf16 v[122:125], v[138:141], v[176:179], v[122:125]
	v_mfma_f32_16x16x32_bf16 v[110:113], v[62:65], v[196:199], v[110:113]
	v_mfma_f32_16x16x32_bf16 v[106:109], v[138:141], v[196:199], v[106:109]
	v_mfma_f32_16x16x32_bf16 v[94:97], v[62:65], v[204:207], v[94:97]
	v_mfma_f32_16x16x32_bf16 v[90:93], v[138:141], v[204:207], v[90:93]
	v_mfma_f32_16x16x32_bf16 v[66:69], v[70:73], v[172:175], v[66:69]
	v_mfma_f32_16x16x32_bf16 v[38:41], v[158:161], v[172:175], v[38:41]
	v_mfma_f32_16x16x32_bf16 v[126:129], v[70:73], v[180:183], v[126:129]
	v_mfma_f32_16x16x32_bf16 v[122:125], v[158:161], v[180:183], v[122:125]
	v_mfma_f32_16x16x32_bf16 v[110:113], v[70:73], v[200:203], v[110:113]
	v_mfma_f32_16x16x32_bf16 v[106:109], v[158:161], v[200:203], v[106:109]
	v_mfma_f32_16x16x32_bf16 v[94:97], v[70:73], v[208:211], v[94:97]
	v_mfma_f32_16x16x32_bf16 v[90:93], v[158:161], v[208:211], v[90:93]
	s_setprio 0
	s_barrier
	s_add_i32 s12, 0, 0x1c000
	s_add_i32 s13, s52, s17
	v_add_u32_e32 v0, s12, v165
	v_lshl_add_u64 v[162:163], v[162:163], 0, s[44:45]
	s_mov_b32 m0, s13
	ds_read_b128 v[212:215], v0
	ds_read_b128 v[216:219], v0 offset:1024
	ds_read_b128 v[220:223], v0 offset:2048
	ds_read_b128 v[224:227], v0 offset:3072
	global_load_lds_dwordx4 v[162:163], off
	v_lshl_add_u64 v[162:163], v[184:185], 0, s[44:45]
	s_add_i32 m0, s13, 0x2000
	s_nop 0
	global_load_lds_dwordx4 v[162:163], off
	s_barrier
	s_waitcnt lgkmcnt(0)
	s_setprio 1
	s_waitcnt lgkmcnt(0)
	v_mfma_f32_16x16x32_bf16 v[134:137], v[212:215], v[168:171], v[134:137]
	v_mfma_f32_16x16x32_bf16 v[130:133], v[220:223], v[168:171], v[130:133]
	v_mfma_f32_16x16x32_bf16 v[118:121], v[212:215], v[176:179], v[118:121]
	v_mfma_f32_16x16x32_bf16 v[114:117], v[220:223], v[176:179], v[114:117]
	v_mfma_f32_16x16x32_bf16 v[102:105], v[212:215], v[196:199], v[102:105]
	v_mfma_f32_16x16x32_bf16 v[98:101], v[220:223], v[196:199], v[98:101]
	v_mfma_f32_16x16x32_bf16 v[86:89], v[212:215], v[204:207], v[86:89]
	v_mfma_f32_16x16x32_bf16 v[82:85], v[220:223], v[204:207], v[82:85]
	v_mfma_f32_16x16x32_bf16 v[134:137], v[216:219], v[172:175], v[134:137]
	v_mfma_f32_16x16x32_bf16 v[130:133], v[224:227], v[172:175], v[130:133]
	v_mfma_f32_16x16x32_bf16 v[118:121], v[216:219], v[180:183], v[118:121]
	v_mfma_f32_16x16x32_bf16 v[114:117], v[224:227], v[180:183], v[114:117]
	v_mfma_f32_16x16x32_bf16 v[102:105], v[216:219], v[200:203], v[102:105]
	v_mfma_f32_16x16x32_bf16 v[98:101], v[224:227], v[200:203], v[98:101]
	v_mfma_f32_16x16x32_bf16 v[86:89], v[216:219], v[208:211], v[86:89]
	v_mfma_f32_16x16x32_bf16 v[82:85], v[224:227], v[208:211], v[82:85]
	s_setprio 0
	s_mov_b32 m0, s28
	v_lshl_add_u64 v[162:163], s[10:11], 0, v[142:143]
	s_barrier
	ds_read_b128 v[168:171], v166 offset:49152
	ds_read_b128 v[172:175], v166 offset:50176
	ds_read_b128 v[176:179], v166 offset:51200
	ds_read_b128 v[180:183], v166 offset:52224
	ds_read_b128 v[196:199], v166 offset:53248
	ds_read_b128 v[200:203], v166 offset:54272
	ds_read_b128 v[204:207], v166 offset:55296
	ds_read_b128 v[208:211], v166 offset:56320
	global_load_lds_dwordx4 v[162:163], off
	v_lshl_add_u64 v[162:163], s[10:11], 0, v[146:147]
	s_mov_b32 m0, s29
	s_nop 0
	global_load_lds_dwordx4 v[162:163], off
	s_barrier
	s_waitcnt lgkmcnt(0)
	s_setprio 1
	s_waitcnt lgkmcnt(0)
	v_mfma_f32_16x16x32_bf16 v[78:81], v[62:65], v[168:171], v[78:81]
	v_mfma_f32_16x16x32_bf16 v[74:77], v[138:141], v[168:171], v[74:77]
	v_mfma_f32_16x16x32_bf16 v[58:61], v[62:65], v[176:179], v[58:61]
	v_mfma_f32_16x16x32_bf16 v[50:53], v[138:141], v[176:179], v[50:53]
	v_mfma_f32_16x16x32_bf16 v[30:33], v[62:65], v[196:199], v[30:33]
	v_mfma_f32_16x16x32_bf16 v[26:29], v[138:141], v[196:199], v[26:29]
	v_mfma_f32_16x16x32_bf16 v[14:17], v[62:65], v[204:207], v[14:17]
	v_mfma_f32_16x16x32_bf16 v[10:13], v[138:141], v[204:207], v[10:13]
	v_mfma_f32_16x16x32_bf16 v[78:81], v[70:73], v[172:175], v[78:81]
	v_mfma_f32_16x16x32_bf16 v[74:77], v[158:161], v[172:175], v[74:77]
	v_mfma_f32_16x16x32_bf16 v[58:61], v[70:73], v[180:183], v[58:61]
	v_mfma_f32_16x16x32_bf16 v[50:53], v[158:161], v[180:183], v[50:53]
	v_mfma_f32_16x16x32_bf16 v[30:33], v[70:73], v[200:203], v[30:33]
	v_mfma_f32_16x16x32_bf16 v[26:29], v[158:161], v[200:203], v[26:29]
	v_mfma_f32_16x16x32_bf16 v[14:17], v[70:73], v[208:211], v[14:17]
	v_mfma_f32_16x16x32_bf16 v[10:13], v[158:161], v[208:211], v[10:13]
	s_setprio 0
	s_barrier
	s_add_u32 s8, s8, 0x80080
	s_addc_u32 s9, s9, 0
	s_add_i32 s10, s12, s17
	v_lshl_add_u64 v[62:63], s[8:9], 0, v[144:145]
	s_mov_b32 m0, s10
	s_nop 0
	global_load_lds_dwordx4 v[62:63], off
	v_lshl_add_u64 v[62:63], s[8:9], 0, v[148:149]
	s_add_i32 m0, s10, 0x2000
	s_nop 0
	global_load_lds_dwordx4 v[62:63], off
	s_waitcnt vmcnt(6)
	s_barrier
; #define PG8_MMA(ai, bj, At, Bt) do { __builtin_amdgcn_s_setprio(1); _Pragma("unroll") for (int m = 0; m < 4; ++m) _Pragma("unroll") for (int n = 0; n < 2; ++n) _Pragma("unroll") for (int k = 0; k < 2; ++k) \
;         acc[ai][bj][m][n] = __builtin_amdgcn_mfma_f32_16x16x32_bf16(Bt[n][k], At[m][k], acc[ai][bj][m][n], 0, 0, 0); __builtin_amdgcn_s_setprio(0); } while (0)
; #define PG8_WAIT_V(n) asm volatile("s_waitcnt vmcnt(" #n ")" ::: "memory")
; #define PG8_BAR __builtin_amdgcn_s_barrier()
; template <class Epi>
; __device__ __forceinline__ void gemm_phase(LAS unsigned char* lds, const int tid, const Gemm g, const Sched& S, const Epi& E) {
;     ...
;             PG8_WAIT_V(6); PG8_BAR; PG8_MMA(1, 1, At, B1); PG8_BAR;
;         }
;         bool keep = false;
;         if constexpr (!epi_after_drain<Epi>::value) keep = E(acc, cur, wr, wc, fr, fq);
	s_setprio 1
	v_mfma_f32_16x16x32_bf16 v[46:49], v[212:215], v[168:171], v[46:49]
	v_mfma_f32_16x16x32_bf16 v[70:73], v[216:219], v[172:175], v[46:49]
	v_mfma_f32_16x16x32_bf16 v[46:49], v[220:223], v[168:171], v[54:57]
	v_mfma_f32_16x16x32_bf16 v[42:45], v[212:215], v[176:179], v[42:45]
	v_mfma_f32_16x16x32_bf16 v[34:37], v[220:223], v[176:179], v[34:37]
	v_mfma_f32_16x16x32_bf16 v[22:25], v[212:215], v[196:199], v[22:25]
	v_mfma_f32_16x16x32_bf16 v[18:21], v[220:223], v[196:199], v[18:21]
	v_mfma_f32_16x16x32_bf16 v[6:9], v[212:215], v[204:207], v[6:9]
	v_mfma_f32_16x16x32_bf16 v[2:5], v[220:223], v[204:207], v[2:5]
	v_mfma_f32_16x16x32_bf16 v[62:65], v[224:227], v[172:175], v[46:49]
	v_mfma_f32_16x16x32_bf16 v[42:45], v[216:219], v[180:183], v[42:45]
	v_mfma_f32_16x16x32_bf16 v[34:37], v[224:227], v[180:183], v[34:37]
	v_mfma_f32_16x16x32_bf16 v[22:25], v[216:219], v[200:203], v[22:25]
	v_mfma_f32_16x16x32_bf16 v[18:21], v[224:227], v[200:203], v[18:21]
	v_mfma_f32_16x16x32_bf16 v[6:9], v[216:219], v[208:211], v[6:9]
	v_mfma_f32_16x16x32_bf16 v[2:5], v[224:227], v[208:211], v[2:5]
	s_setprio 0
	s_add_i32 s51, s51, 2
	s_add_u32 s49, s49, 0x100
	s_addc_u32 s50, s50, 0
	s_add_u32 s6, s6, 0x4000
	s_addc_u32 s7, s7, 0
	s_cmp_gt_u32 s51, 29
	s_barrier
	s_cbranch_scc0 .LBB0_489
	v_readlane_b32 s6, v251, 0
	s_cmp_lt_u32 s6, 16
	s_cbranch_scc1 .Lsk_A
	v_readlane_b32 s8, v253, 52
	v_readlane_b32 s9, v253, 53
	s_and_b32 s6, s6, 15
	s_lshl_b32 s6, s6, 18
	s_add_u32 s8, s8, s6
	s_addc_u32 s9, s9, 0
	s_add_u32 s8, s8, 0x1af00000
	s_addc_u32 s9, s9, 0
	v_lshlrev_b32_e32 v158, 4, v151
	global_store_dwordx4 v158, v[2:5], s[8:9]
	s_add_u32 s8, s8, 0x2000
	s_addc_u32 s9, s9, 0
	global_store_dwordx4 v158, v[6:9], s[8:9]
	s_add_u32 s8, s8, 0x2000
	s_addc_u32 s9, s9, 0
	global_store_dwordx4 v158, v[10:13], s[8:9]
	s_add_u32 s8, s8, 0x2000
	s_addc_u32 s9, s9, 0
	global_store_dwordx4 v158, v[14:17], s[8:9]
	s_add_u32 s8, s8, 0x2000
	s_addc_u32 s9, s9, 0
	global_store_dwordx4 v158, v[18:21], s[8:9]
	s_add_u32 s8, s8, 0x2000
	s_addc_u32 s9, s9, 0
	global_store_dwordx4 v158, v[22:25], s[8:9]
	s_add_u32 s8, s8, 0x2000
	s_addc_u32 s9, s9, 0
	global_store_dwordx4 v158, v[26:29], s[8:9]
	s_add_u32 s8, s8, 0x2000
	s_addc_u32 s9, s9, 0
	global_store_dwordx4 v158, v[30:33], s[8:9]
	s_add_u32 s8, s8, 0x2000
	s_addc_u32 s9, s9, 0
	global_store_dwordx4 v158, v[34:37], s[8:9]
	s_add_u32 s8, s8, 0x2000
	s_addc_u32 s9, s9, 0
	global_store_dwordx4 v158, v[38:41], s[8:9]
	s_add_u32 s8, s8, 0x2000
	s_addc_u32 s9, s9, 0
	global_store_dwordx4 v158, v[42:45], s[8:9]
	s_add_u32 s8, s8, 0x2000
	s_addc_u32 s9, s9, 0
	global_store_dwordx4 v158, v[50:53], s[8:9]
	s_add_u32 s8, s8, 0x2000
	s_addc_u32 s9, s9, 0
	global_store_dwordx4 v158, v[58:61], s[8:9]
	s_add_u32 s8, s8, 0x2000
	s_addc_u32 s9, s9, 0
	global_store_dwordx4 v158, v[62:65], s[8:9]
	s_add_u32 s8, s8, 0x2000
	s_addc_u32 s9, s9, 0
	global_store_dwordx4 v158, v[66:69], s[8:9]
	s_add_u32 s8, s8, 0x2000
	s_addc_u32 s9, s9, 0
	global_store_dwordx4 v158, v[70:73], s[8:9]
	s_add_u32 s8, s8, 0x2000
	s_addc_u32 s9, s9, 0
	global_store_dwordx4 v158, v[74:77], s[8:9]
	s_add_u32 s8, s8, 0x2000
	s_addc_u32 s9, s9, 0
	global_store_dwordx4 v158, v[78:81], s[8:9]
	s_add_u32 s8, s8, 0x2000
	s_addc_u32 s9, s9, 0
	global_store_dwordx4 v158, v[82:85], s[8:9]
	s_add_u32 s8, s8, 0x2000
	s_addc_u32 s9, s9, 0
	global_store_dwordx4 v158, v[86:89], s[8:9]
	s_add_u32 s8, s8, 0x2000
	s_addc_u32 s9, s9, 0
	global_store_dwordx4 v158, v[90:93], s[8:9]
	s_add_u32 s8, s8, 0x2000
	s_addc_u32 s9, s9, 0
	global_store_dwordx4 v158, v[94:97], s[8:9]
	s_add_u32 s8, s8, 0x2000
	s_addc_u32 s9, s9, 0
	global_store_dwordx4 v158, v[98:101], s[8:9]
	s_add_u32 s8, s8, 0x2000
	s_addc_u32 s9, s9, 0
	global_store_dwordx4 v158, v[102:105], s[8:9]
	s_add_u32 s8, s8, 0x2000
	s_addc_u32 s9, s9, 0
	global_store_dwordx4 v158, v[106:109], s[8:9]
	s_add_u32 s8, s8, 0x2000
	s_addc_u32 s9, s9, 0
	global_store_dwordx4 v158, v[110:113], s[8:9]
	s_add_u32 s8, s8, 0x2000
	s_addc_u32 s9, s9, 0
	global_store_dwordx4 v158, v[114:117], s[8:9]
	s_add_u32 s8, s8, 0x2000
	s_addc_u32 s9, s9, 0
	global_store_dwordx4 v158, v[118:121], s[8:9]
	s_add_u32 s8, s8, 0x2000
	s_addc_u32 s9, s9, 0
	global_store_dwordx4 v158, v[122:125], s[8:9]
	s_add_u32 s8, s8, 0x2000
	s_addc_u32 s9, s9, 0
	global_store_dwordx4 v158, v[126:129], s[8:9]
	s_add_u32 s8, s8, 0x2000
	s_addc_u32 s9, s9, 0
	global_store_dwordx4 v158, v[130:133], s[8:9]
	s_add_u32 s8, s8, 0x2000
	s_addc_u32 s9, s9, 0
	global_store_dwordx4 v158, v[134:137], s[8:9]
	s_waitcnt vmcnt(0)
	buffer_wbl2 sc1
	s_waitcnt vmcnt(0)
	s_branch .Lsk_bdone
.Lsk_A:
	v_readlane_b32 s6, v251, 0
	s_and_b32 s6, s6, 15
	s_lshl_b32 s6, s6, 6
	s_addk_i32 s6, 0x4000
	v_readlane_b32 s11, v252, 29
	v_readlane_b32 s13, v252, 30
	s_add_u32 s11, s11, s6
	s_addc_u32 s13, s13, 0
	v_mov_b32_e32 v160, s11
	v_mov_b32_e32 v161, s13
	v_readlane_b32 s11, v254, 27
	v_readlane_b32 s13, v254, 29
	s_lshr_b32 s11, s11, 4
	s_add_i32 s11, s11, s13
	s_add_i32 s11, s11, 1
	v_mov_b32_e32 v162, s11
	v_readlane_b32 s6, v251, 0
	v_readlane_b32 s8, v253, 52
	v_readlane_b32 s9, v253, 53
	s_and_b32 s6, s6, 15
	s_lshl_b32 s6, s6, 18
	s_add_u32 s8, s8, s6
	s_addc_u32 s9, s9, 0
	s_add_u32 s8, s8, 0x1af00000
	s_addc_u32 s9, s9, 0
	v_lshlrev_b32_e32 v158, 4, v151
	s_mov_b64 s[6:7], exec
	s_mov_b64 exec, 1
	s_mov_b32 s11, 0
.Lsk_spin:
	global_load_dword v159, v[160:161], off sc1
	s_waitcnt vmcnt(0)
	v_cmp_ge_u32_e32 vcc, v159, v162
	s_cbranch_vccnz .Lsk_go
	s_sleep 1
	s_add_i32 s11, s11, 1
	s_cmp_lt_u32 s11, 0x100000
	s_cbranch_scc1 .Lsk_spin
; template <class Epi>
; __device__ __forceinline__ void gemm_phase(LAS unsigned char* lds, const int tid, const Gemm g, const Sched& S, const Epi& E) {
;     ...
;         if constexpr (!epi_after_drain<Epi>::value) keep = E(acc, cur, wr, wc, fr, fq);
.Lsk_go:
	s_mov_b64 exec, s[6:7]
	buffer_inv sc1
	global_load_dwordx4 v[196:199], v158, s[8:9]
	s_add_u32 s8, s8, 0x2000
	s_addc_u32 s9, s9, 0
	global_load_dwordx4 v[200:203], v158, s[8:9]
	s_add_u32 s8, s8, 0x2000
	s_addc_u32 s9, s9, 0
	global_load_dwordx4 v[204:207], v158, s[8:9]
	s_add_u32 s8, s8, 0x2000
	s_addc_u32 s9, s9, 0
	global_load_dwordx4 v[208:211], v158, s[8:9]
	s_add_u32 s8, s8, 0x2000
	s_addc_u32 s9, s9, 0
	global_load_dwordx4 v[212:215], v158, s[8:9]
	s_add_u32 s8, s8, 0x2000
	s_addc_u32 s9, s9, 0
	global_load_dwordx4 v[46:49], v158, s[8:9]
	s_add_u32 s8, s8, 0x2000
	s_addc_u32 s9, s9, 0
	global_load_dwordx4 v[54:57], v158, s[8:9]
	s_add_u32 s8, s8, 0x2000
	s_addc_u32 s9, s9, 0
	global_load_dwordx4 v[138:141], v158, s[8:9]
	s_add_u32 s8, s8, 0x2000
	s_addc_u32 s9, s9, 0
	s_waitcnt vmcnt(7)
	v_pk_add_f32 v[2:3], v[2:3], v[196:197]
	v_pk_add_f32 v[4:5], v[4:5], v[198:199]
	s_waitcnt vmcnt(6)
	v_pk_add_f32 v[6:7], v[6:7], v[200:201]
	v_pk_add_f32 v[8:9], v[8:9], v[202:203]
	s_waitcnt vmcnt(5)
	v_pk_add_f32 v[10:11], v[10:11], v[204:205]
	v_pk_add_f32 v[12:13], v[12:13], v[206:207]
	s_waitcnt vmcnt(4)
	v_pk_add_f32 v[14:15], v[14:15], v[208:209]
	v_pk_add_f32 v[16:17], v[16:17], v[210:211]
	s_waitcnt vmcnt(3)
	v_pk_add_f32 v[18:19], v[18:19], v[212:213]
	v_pk_add_f32 v[20:21], v[20:21], v[214:215]
	s_waitcnt vmcnt(2)
	v_pk_add_f32 v[22:23], v[22:23], v[46:47]
	v_pk_add_f32 v[24:25], v[24:25], v[48:49]
	s_waitcnt vmcnt(1)
	v_pk_add_f32 v[26:27], v[26:27], v[54:55]
	v_pk_add_f32 v[28:29], v[28:29], v[56:57]
	s_waitcnt vmcnt(0)
	v_pk_add_f32 v[30:31], v[30:31], v[138:139]
	v_pk_add_f32 v[32:33], v[32:33], v[140:141]
	global_load_dwordx4 v[196:199], v158, s[8:9]
	s_add_u32 s8, s8, 0x2000
	s_addc_u32 s9, s9, 0
	global_load_dwordx4 v[200:203], v158, s[8:9]
	s_add_u32 s8, s8, 0x2000
	s_addc_u32 s9, s9, 0
	global_load_dwordx4 v[204:207], v158, s[8:9]
	s_add_u32 s8, s8, 0x2000
	s_addc_u32 s9, s9, 0
	global_load_dwordx4 v[208:211], v158, s[8:9]
	s_add_u32 s8, s8, 0x2000
	s_addc_u32 s9, s9, 0
	global_load_dwordx4 v[212:215], v158, s[8:9]
	s_add_u32 s8, s8, 0x2000
	s_addc_u32 s9, s9, 0
	global_load_dwordx4 v[46:49], v158, s[8:9]
	s_add_u32 s8, s8, 0x2000
	s_addc_u32 s9, s9, 0
	global_load_dwordx4 v[54:57], v158, s[8:9]
	s_add_u32 s8, s8, 0x2000
	s_addc_u32 s9, s9, 0
	global_load_dwordx4 v[138:141], v158, s[8:9]
	s_add_u32 s8, s8, 0x2000
	s_addc_u32 s9, s9, 0
	s_waitcnt vmcnt(7)
	v_pk_add_f32 v[34:35], v[34:35], v[196:197]
	v_pk_add_f32 v[36:37], v[36:37], v[198:199]
	s_waitcnt vmcnt(6)
	v_pk_add_f32 v[38:39], v[38:39], v[200:201]
	v_pk_add_f32 v[40:41], v[40:41], v[202:203]
	s_waitcnt vmcnt(5)
	v_pk_add_f32 v[42:43], v[42:43], v[204:205]
	v_pk_add_f32 v[44:45], v[44:45], v[206:207]
	s_waitcnt vmcnt(4)
	v_pk_add_f32 v[50:51], v[50:51], v[208:209]
	v_pk_add_f32 v[52:53], v[52:53], v[210:211]
	s_waitcnt vmcnt(3)
	v_pk_add_f32 v[58:59], v[58:59], v[212:213]
	v_pk_add_f32 v[60:61], v[60:61], v[214:215]
	s_waitcnt vmcnt(2)
	v_pk_add_f32 v[62:63], v[62:63], v[46:47]
	v_pk_add_f32 v[64:65], v[64:65], v[48:49]
	s_waitcnt vmcnt(1)
	v_pk_add_f32 v[66:67], v[66:67], v[54:55]
	v_pk_add_f32 v[68:69], v[68:69], v[56:57]
	s_waitcnt vmcnt(0)
	v_pk_add_f32 v[70:71], v[70:71], v[138:139]
	v_pk_add_f32 v[72:73], v[72:73], v[140:141]
	global_load_dwordx4 v[196:199], v158, s[8:9]
	s_add_u32 s8, s8, 0x2000
	s_addc_u32 s9, s9, 0
	global_load_dwordx4 v[200:203], v158, s[8:9]
	s_add_u32 s8, s8, 0x2000
	s_addc_u32 s9, s9, 0
	global_load_dwordx4 v[204:207], v158, s[8:9]
	s_add_u32 s8, s8, 0x2000
	s_addc_u32 s9, s9, 0
	global_load_dwordx4 v[208:211], v158, s[8:9]
	s_add_u32 s8, s8, 0x2000
	s_addc_u32 s9, s9, 0
	global_load_dwordx4 v[212:215], v158, s[8:9]
	s_add_u32 s8, s8, 0x2000
	s_addc_u32 s9, s9, 0
	global_load_dwordx4 v[46:49], v158, s[8:9]
	s_add_u32 s8, s8, 0x2000
	s_addc_u32 s9, s9, 0
	global_load_dwordx4 v[54:57], v158, s[8:9]
	s_add_u32 s8, s8, 0x2000
	s_addc_u32 s9, s9, 0
	global_load_dwordx4 v[138:141], v158, s[8:9]
	s_add_u32 s8, s8, 0x2000
	s_addc_u32 s9, s9, 0
	s_waitcnt vmcnt(7)
	v_pk_add_f32 v[74:75], v[74:75], v[196:197]
	v_pk_add_f32 v[76:77], v[76:77], v[198:199]
	s_waitcnt vmcnt(6)
	v_pk_add_f32 v[78:79], v[78:79], v[200:201]
	v_pk_add_f32 v[80:81], v[80:81], v[202:203]
	s_waitcnt vmcnt(5)
	v_pk_add_f32 v[82:83], v[82:83], v[204:205]
	v_pk_add_f32 v[84:85], v[84:85], v[206:207]
	s_waitcnt vmcnt(4)
	v_pk_add_f32 v[86:87], v[86:87], v[208:209]
	v_pk_add_f32 v[88:89], v[88:89], v[210:211]
	s_waitcnt vmcnt(3)
	v_pk_add_f32 v[90:91], v[90:91], v[212:213]
	v_pk_add_f32 v[92:93], v[92:93], v[214:215]
	s_waitcnt vmcnt(2)
	v_pk_add_f32 v[94:95], v[94:95], v[46:47]
	v_pk_add_f32 v[96:97], v[96:97], v[48:49]
	s_waitcnt vmcnt(1)
	v_pk_add_f32 v[98:99], v[98:99], v[54:55]
	v_pk_add_f32 v[100:101], v[100:101], v[56:57]
	s_waitcnt vmcnt(0)
	v_pk_add_f32 v[102:103], v[102:103], v[138:139]
	v_pk_add_f32 v[104:105], v[104:105], v[140:141]
	global_load_dwordx4 v[196:199], v158, s[8:9]
	s_add_u32 s8, s8, 0x2000
	s_addc_u32 s9, s9, 0
	global_load_dwordx4 v[200:203], v158, s[8:9]
	s_add_u32 s8, s8, 0x2000
	s_addc_u32 s9, s9, 0
	global_load_dwordx4 v[204:207], v158, s[8:9]
	s_add_u32 s8, s8, 0x2000
	s_addc_u32 s9, s9, 0
	global_load_dwordx4 v[208:211], v158, s[8:9]
	s_add_u32 s8, s8, 0x2000
	s_addc_u32 s9, s9, 0
	global_load_dwordx4 v[212:215], v158, s[8:9]
	s_add_u32 s8, s8, 0x2000
	s_addc_u32 s9, s9, 0
	global_load_dwordx4 v[46:49], v158, s[8:9]
	s_add_u32 s8, s8, 0x2000
	s_addc_u32 s9, s9, 0
	global_load_dwordx4 v[54:57], v158, s[8:9]
	s_add_u32 s8, s8, 0x2000
	s_addc_u32 s9, s9, 0
	global_load_dwordx4 v[138:141], v158, s[8:9]
	s_add_u32 s8, s8, 0x2000
	s_addc_u32 s9, s9, 0
	s_waitcnt vmcnt(7)
; __device__ __forceinline__ unsigned pk2(float lo, float hi) { const f32x2 f = {lo, hi}; const bf16n2 v = __builtin_convertvector(f, bf16n2); return __builtin_bit_cast(unsigned, v); }
; __device__ __forceinline__ float sigmoidf_(float x) { return __builtin_amdgcn_rcpf(1.0f + __expf(-x)); }
;     __device__ __forceinline__ bool operator()(f32x4 (&acc)[2][2][4][2], const Unit& u, int wr, int wc, int fr, int fq) const {
;         const int kv = u.pm >> 3; const int row0 = (u.pm & 7) * BM + wr * 64 + fr; const int col0 = wc * 32 + 8 * fq;
;         float bv[2][8];
; #pragma unroll
;         for (int bj = 0; bj < 2; ++bj)
; #pragma unroll
;             for (int j = 0; j < 8; ++j) bv[bj][j] = bh[kv * 256 + col0 + bj * HALF + j];
; #pragma unroll
;         for (int ai = 0; ai < 2; ++ai)
; #pragma unroll
;             for (int m = 0; m < 4; ++m) { bf16_t* rowp = hid + ((size_t)kv * 2048 + row0 + ai * HALF + m * 16) * 256 + col0;
; #pragma unroll
;                 for (int bj = 0; bj < 2; ++bj) { float o[8];
; #pragma unroll
;                     for (int j = 0; j < 8; ++j) { const float x = acc[ai][bj][m][j >> 2][j & 3] + bv[bj][j];
;                         o[j] = x * sigmoidf_(1.5957691216f * (x + 0.044715f * x * x * x)); }
;                     u32x4 w; w.x = pk2(o[0], o[1]); w.y = pk2(o[2], o[3]); w.z = pk2(o[4], o[5]); w.w = pk2(o[6], o[7]);
;                     *(u32x4*)(rowp + bj * HALF) = w; } }
	v_pk_add_f32 v[106:107], v[106:107], v[196:197]
	v_pk_add_f32 v[108:109], v[108:109], v[198:199]
	s_waitcnt vmcnt(6)
	v_pk_add_f32 v[110:111], v[110:111], v[200:201]
	v_pk_add_f32 v[112:113], v[112:113], v[202:203]
	s_waitcnt vmcnt(5)
	v_pk_add_f32 v[114:115], v[114:115], v[204:205]
	v_pk_add_f32 v[116:117], v[116:117], v[206:207]
	s_waitcnt vmcnt(4)
	v_pk_add_f32 v[118:119], v[118:119], v[208:209]
	v_pk_add_f32 v[120:121], v[120:121], v[210:211]
	s_waitcnt vmcnt(3)
	v_pk_add_f32 v[122:123], v[122:123], v[212:213]
	v_pk_add_f32 v[124:125], v[124:125], v[214:215]
	s_waitcnt vmcnt(2)
	v_pk_add_f32 v[126:127], v[126:127], v[46:47]
	v_pk_add_f32 v[128:129], v[128:129], v[48:49]
	s_waitcnt vmcnt(1)
	v_pk_add_f32 v[130:131], v[130:131], v[54:55]
	v_pk_add_f32 v[132:133], v[132:133], v[56:57]
	s_waitcnt vmcnt(0)
	v_pk_add_f32 v[134:135], v[134:135], v[138:139]
	v_pk_add_f32 v[136:137], v[136:137], v[140:141]
	s_ashr_i32 s6, s22, 3
	s_lshl_b32 s7, s22, 8
	v_lshl_or_b32 v46, s6, 8, v150
	v_readlane_b32 s8, v252, 10
	s_and_b32 s7, s7, 0x700
	v_ashrrev_i32_e32 v47, 31, v46
	v_readlane_b32 s9, v252, 11
	v_lshlrev_b32_e32 v0, 1, v150
	s_mov_b32 s22, s37
	v_lshl_add_u64 v[162:163], v[46:47], 2, s[8:9]
	v_add_u32_e32 v46, s7, v164
	s_ashr_i32 s7, s6, 31
	v_ashrrev_i32_e32 v47, 31, v46
	s_lshl_b64 s[6:7], s[6:7], 20
	v_lshlrev_b64 v[46:47], 9, v[46:47]
	v_lshl_add_u64 v[160:161], v[46:47], 0, s[6:7]
	v_lshl_add_u64 v[46:47], s[78:79], 0, v[160:161]
	v_lshl_add_u64 v[158:159], v[46:47], 0, v[0:1]
	global_load_dwordx4 v[46:49], v[162:163], off offset:16
	global_load_dwordx4 v[54:57], v[162:163], off
	s_mov_b64 s[6:7], 0x10000
	s_mov_b64 s[8:9], s[2:3]
	s_waitcnt vmcnt(0)
	v_pk_add_f32 v[38:39], v[38:39], v[46:47]
	v_pk_add_f32 v[66:67], v[66:67], v[54:55]
	v_pk_add_f32 v[68:69], v[68:69], v[56:57]
	v_mul_f32_e32 v0, 0x3d372713, v66
	v_mul_f32_e32 v0, v66, v0
	v_fma_f32 v0, v66, v0, v66
	v_mul_f32_e32 v0, 0x3fcc422a, v0
	v_mul_f32_e32 v0, 0xbfb8aa3b, v0
	v_exp_f32_e32 v0, v0
	v_pk_add_f32 v[40:41], v[40:41], v[48:49]
	v_pk_add_f32 v[126:127], v[126:127], v[54:55]
	v_pk_add_f32 v[128:129], v[128:129], v[56:57]
	v_add_f32_e32 v0, 1.0, v0
	v_rcp_f32_e32 v138, v0
	v_mul_f32_e32 v0, 0x3d372713, v67
	v_mul_f32_e32 v0, v67, v0
	v_fma_f32 v0, v67, v0, v67
	v_mul_f32_e32 v0, 0x3fcc422a, v0
	v_mul_f32_e32 v0, 0xbfb8aa3b, v0
	v_exp_f32_e32 v0, v0
	v_pk_add_f32 v[122:123], v[122:123], v[46:47]
	v_pk_add_f32 v[110:111], v[110:111], v[54:55]
	v_pk_add_f32 v[112:113], v[112:113], v[56:57]
	v_add_f32_e32 v0, 1.0, v0
	v_rcp_f32_e32 v139, v0
	v_mul_f32_e32 v0, 0x3d372713, v68
	v_mul_f32_e32 v0, v68, v0
	v_fma_f32 v0, v68, v0, v68
	v_mul_f32_e32 v0, 0x3fcc422a, v0
	v_mul_f32_e32 v0, 0xbfb8aa3b, v0
	v_exp_f32_e32 v0, v0
	v_pk_mul_f32 v[66:67], v[66:67], v[138:139]
	v_pk_add_f32 v[106:107], v[106:107], v[46:47]
	v_pk_add_f32 v[94:95], v[94:95], v[54:55]
	v_add_f32_e32 v0, 1.0, v0
	v_rcp_f32_e32 v138, v0
	v_mul_f32_e32 v0, 0x3d372713, v69
	v_mul_f32_e32 v0, v69, v0
	v_fma_f32 v0, v69, v0, v69
	v_mul_f32_e32 v0, 0x3fcc422a, v0
	v_mul_f32_e32 v0, 0xbfb8aa3b, v0
	v_exp_f32_e32 v0, v0
	v_pk_add_f32 v[96:97], v[96:97], v[56:57]
	v_pk_add_f32 v[90:91], v[90:91], v[46:47]
	v_pk_add_f32 v[78:79], v[78:79], v[54:55]
	v_add_f32_e32 v0, 1.0, v0
	v_rcp_f32_e32 v139, v0
	v_mul_f32_e32 v0, 0x3d372713, v38
	v_mul_f32_e32 v0, v38, v0
	v_fma_f32 v0, v38, v0, v38
	v_mul_f32_e32 v0, 0x3fcc422a, v0
	v_mul_f32_e32 v0, 0xbfb8aa3b, v0
	v_exp_f32_e32 v0, v0
	v_pk_mul_f32 v[68:69], v[68:69], v[138:139]
	v_pk_add_f32 v[80:81], v[80:81], v[56:57]
	v_pk_add_f32 v[74:75], v[74:75], v[46:47]
	v_add_f32_e32 v0, 1.0, v0
	v_rcp_f32_e32 v138, v0
	v_mul_f32_e32 v0, 0x3d372713, v39
	v_mul_f32_e32 v0, v39, v0
	v_fma_f32 v0, v39, v0, v39
	v_mul_f32_e32 v0, 0x3fcc422a, v0
	v_mul_f32_e32 v0, 0xbfb8aa3b, v0
	v_exp_f32_e32 v0, v0
	v_pk_add_f32 v[58:59], v[58:59], v[54:55]
	v_pk_add_f32 v[60:61], v[60:61], v[56:57]
	v_pk_add_f32 v[50:51], v[50:51], v[46:47]
	v_add_f32_e32 v0, 1.0, v0
	v_rcp_f32_e32 v139, v0
	v_mul_f32_e32 v0, 0x3d372713, v40
	v_mul_f32_e32 v0, v40, v0
	v_fma_f32 v0, v40, v0, v40
	v_mul_f32_e32 v0, 0x3fcc422a, v0
	v_mul_f32_e32 v0, 0xbfb8aa3b, v0
	v_exp_f32_e32 v0, v0
	v_pk_mul_f32 v[38:39], v[38:39], v[138:139]
	v_pk_add_f32 v[30:31], v[30:31], v[54:55]
	v_cvt_pk_bf16_f32 v140, v38, v39
	v_add_f32_e32 v0, 1.0, v0
	v_rcp_f32_e32 v138, v0
	v_mul_f32_e32 v0, 0x3d372713, v41
	v_mul_f32_e32 v0, v41, v0
	v_fma_f32 v0, v41, v0, v41
	v_mul_f32_e32 v0, 0x3fcc422a, v0
	v_mul_f32_e32 v0, 0xbfb8aa3b, v0
	v_exp_f32_e32 v0, v0
	v_pk_add_f32 v[32:33], v[32:33], v[56:57]
	v_pk_add_f32 v[26:27], v[26:27], v[46:47]
	v_pk_add_f32 v[14:15], v[14:15], v[54:55]
	v_add_f32_e32 v0, 1.0, v0
	v_rcp_f32_e32 v139, v0
	v_pk_add_f32 v[16:17], v[16:17], v[56:57]
	v_pk_add_f32 v[10:11], v[10:11], v[46:47]
	v_pk_mul_f32 v[40:41], v[40:41], v[138:139]
	v_cvt_pk_bf16_f32 v138, v66, v67
	v_cvt_pk_bf16_f32 v139, v68, v69
	v_cvt_pk_bf16_f32 v141, v40, v41
	global_load_dwordx4 v[38:41], v[162:163], off offset:528
	global_load_dwordx4 v[66:69], v[162:163], off offset:512
	s_waitcnt vmcnt(0)
; __device__ __forceinline__ unsigned pk2(float lo, float hi) { const f32x2 f = {lo, hi}; const bf16n2 v = __builtin_convertvector(f, bf16n2); return __builtin_bit_cast(unsigned, v); }
; __device__ __forceinline__ float sigmoidf_(float x) { return __builtin_amdgcn_rcpf(1.0f + __expf(-x)); }
;     __device__ __forceinline__ bool operator()(f32x4 (&acc)[2][2][4][2], const Unit& u, int wr, int wc, int fr, int fq) const {
;     ...
;         for (int ai = 0; ai < 2; ++ai)
; #pragma unroll
;             for (int m = 0; m < 4; ++m) { bf16_t* rowp = hid + ((size_t)kv * 2048 + row0 + ai * HALF + m * 16) * 256 + col0;
; #pragma unroll
;                 for (int bj = 0; bj < 2; ++bj) { float o[8];
; #pragma unroll
;                     for (int j = 0; j < 8; ++j) { const float x = acc[ai][bj][m][j >> 2][j & 3] + bv[bj][j];
;                         o[j] = x * sigmoidf_(1.5957691216f * (x + 0.044715f * x * x * x)); }
;                     u32x4 w; w.x = pk2(o[0], o[1]); w.y = pk2(o[2], o[3]); w.z = pk2(o[4], o[5]); w.w = pk2(o[6], o[7]);
;                     *(u32x4*)(rowp + bj * HALF) = w; } }
	v_pk_add_f32 v[130:131], v[130:131], v[38:39]
	v_pk_add_f32 v[134:135], v[134:135], v[66:67]
	v_pk_add_f32 v[136:137], v[136:137], v[68:69]
	v_mul_f32_e32 v0, 0x3d372713, v134
	v_mul_f32_e32 v0, v134, v0
	v_fma_f32 v0, v134, v0, v134
	v_mul_f32_e32 v0, 0x3fcc422a, v0
	v_mul_f32_e32 v0, 0xbfb8aa3b, v0
	v_exp_f32_e32 v0, v0
	global_store_dwordx4 v[158:159], v[138:141], off
	v_pk_add_f32 v[118:119], v[118:119], v[66:67]
	v_pk_add_f32 v[120:121], v[120:121], v[68:69]
	v_add_f32_e32 v0, 1.0, v0
	v_rcp_f32_e32 v162, v0
	v_mul_f32_e32 v0, 0x3d372713, v135
	v_mul_f32_e32 v0, v135, v0
	v_fma_f32 v0, v135, v0, v135
	v_mul_f32_e32 v0, 0x3fcc422a, v0
	v_mul_f32_e32 v0, 0xbfb8aa3b, v0
	v_exp_f32_e32 v0, v0
	v_pk_add_f32 v[114:115], v[114:115], v[38:39]
	v_pk_add_f32 v[102:103], v[102:103], v[66:67]
	v_pk_add_f32 v[104:105], v[104:105], v[68:69]
	v_add_f32_e32 v0, 1.0, v0
	v_rcp_f32_e32 v163, v0
	v_mul_f32_e32 v0, 0x3d372713, v136
	v_mul_f32_e32 v0, v136, v0
	v_fma_f32 v0, v136, v0, v136
	v_mul_f32_e32 v0, 0x3fcc422a, v0
	v_mul_f32_e32 v0, 0xbfb8aa3b, v0
	v_exp_f32_e32 v0, v0
	v_pk_mul_f32 v[134:135], v[134:135], v[162:163]
	v_pk_add_f32 v[98:99], v[98:99], v[38:39]
	v_pk_add_f32 v[86:87], v[86:87], v[66:67]
	v_add_f32_e32 v0, 1.0, v0
	v_rcp_f32_e32 v162, v0
	v_mul_f32_e32 v0, 0x3d372713, v137
	v_mul_f32_e32 v0, v137, v0
	v_fma_f32 v0, v137, v0, v137
	v_mul_f32_e32 v0, 0x3fcc422a, v0
	v_mul_f32_e32 v0, 0xbfb8aa3b, v0
	v_exp_f32_e32 v0, v0
	v_pk_add_f32 v[88:89], v[88:89], v[68:69]
	v_pk_add_f32 v[82:83], v[82:83], v[38:39]
	v_pk_add_f32 v[70:71], v[70:71], v[66:67]
	v_add_f32_e32 v0, 1.0, v0
	v_rcp_f32_e32 v163, v0
	v_mul_f32_e32 v0, 0x3d372713, v130
	v_mul_f32_e32 v0, v130, v0
	v_fma_f32 v0, v130, v0, v130
	v_mul_f32_e32 v0, 0x3fcc422a, v0
	v_mul_f32_e32 v0, 0xbfb8aa3b, v0
	v_exp_f32_e32 v0, v0
	v_pk_mul_f32 v[136:137], v[136:137], v[162:163]
	v_pk_add_f32 v[72:73], v[72:73], v[68:69]
	v_pk_add_f32 v[62:63], v[62:63], v[38:39]
	v_add_f32_e32 v0, 1.0, v0
	v_rcp_f32_e32 v162, v0
	v_mul_f32_e32 v0, 0x3d372713, v131
	v_mul_f32_e32 v0, v131, v0
	v_fma_f32 v0, v131, v0, v131
	v_mul_f32_e32 v0, 0x3fcc422a, v0
	v_mul_f32_e32 v0, 0xbfb8aa3b, v0
	v_exp_f32_e32 v0, v0
	v_pk_add_f32 v[42:43], v[42:43], v[66:67]
	v_pk_add_f32 v[44:45], v[44:45], v[68:69]
	v_pk_add_f32 v[34:35], v[34:35], v[38:39]
	v_add_f32_e32 v0, 1.0, v0
	v_rcp_f32_e32 v163, v0
	v_pk_add_f32 v[22:23], v[22:23], v[66:67]
	v_pk_add_f32 v[24:25], v[24:25], v[68:69]
	v_pk_add_f32 v[18:19], v[18:19], v[38:39]
	v_pk_mul_f32 v[162:163], v[130:131], v[162:163]
	v_pk_add_f32 v[130:131], v[132:133], v[40:41]
	v_pk_add_f32 v[6:7], v[6:7], v[66:67]
	v_mul_f32_e32 v0, 0x3d372713, v130
	v_mul_f32_e32 v0, v130, v0
	v_fma_f32 v0, v130, v0, v130
	v_mul_f32_e32 v0, 0x3fcc422a, v0
	v_mul_f32_e32 v0, 0xbfb8aa3b, v0
	v_exp_f32_e32 v0, v0
	v_pk_add_f32 v[8:9], v[8:9], v[68:69]
	v_pk_add_f32 v[2:3], v[2:3], v[38:39]
	v_add_f32_e32 v0, 1.0, v0
	v_rcp_f32_e32 v132, v0
	v_mul_f32_e32 v0, 0x3d372713, v131
	v_mul_f32_e32 v0, v131, v0
	v_fma_f32 v0, v131, v0, v131
	v_mul_f32_e32 v0, 0x3fcc422a, v0
	v_mul_f32_e32 v0, 0xbfb8aa3b, v0
	v_exp_f32_e32 v0, v0
	s_nop 0
	v_add_f32_e32 v0, 1.0, v0
	v_rcp_f32_e32 v133, v0
	v_mul_f32_e32 v0, 0x3d372713, v126
	v_mul_f32_e32 v0, v126, v0
	v_fma_f32 v0, v126, v0, v126
	v_mul_f32_e32 v0, 0x3fcc422a, v0
	v_mul_f32_e32 v0, 0xbfb8aa3b, v0
	v_exp_f32_e32 v0, v0
	v_pk_mul_f32 v[138:139], v[130:131], v[132:133]
	v_cvt_pk_bf16_f32 v130, v134, v135
	v_cvt_pk_bf16_f32 v131, v136, v137
	v_cvt_pk_bf16_f32 v132, v162, v163
	v_cvt_pk_bf16_f32 v133, v138, v139
	v_add_f32_e32 v0, 1.0, v0
	global_store_dwordx4 v[158:159], v[130:133], off offset:256
	s_nop 1
	v_rcp_f32_e32 v132, v0
	v_mul_f32_e32 v0, 0x3d372713, v127
	v_mul_f32_e32 v0, v127, v0
	v_fma_f32 v0, v127, v0, v127
	v_mul_f32_e32 v0, 0x3fcc422a, v0
	v_mul_f32_e32 v0, 0xbfb8aa3b, v0
	v_exp_f32_e32 v0, v0
	v_or_b32_e32 v130, 0x2000, v160
	v_mov_b32_e32 v131, v161
	v_lshl_add_u64 v[130:131], v[152:153], 0, v[130:131]
	v_add_f32_e32 v0, 1.0, v0
	v_rcp_f32_e32 v133, v0
	v_mul_f32_e32 v0, 0x3d372713, v128
	v_mul_f32_e32 v0, v128, v0
	v_fma_f32 v0, v128, v0, v128
	v_mul_f32_e32 v0, 0x3fcc422a, v0
	v_mul_f32_e32 v0, 0xbfb8aa3b, v0
	v_exp_f32_e32 v0, v0
	v_pk_mul_f32 v[126:127], v[126:127], v[132:133]
	v_add_f32_e32 v0, 1.0, v0
	v_rcp_f32_e32 v132, v0
	v_mul_f32_e32 v0, 0x3d372713, v129
	v_mul_f32_e32 v0, v129, v0
	v_fma_f32 v0, v129, v0, v129
	v_mul_f32_e32 v0, 0x3fcc422a, v0
	v_mul_f32_e32 v0, 0xbfb8aa3b, v0
	v_exp_f32_e32 v0, v0
	s_nop 0
	v_add_f32_e32 v0, 1.0, v0
	v_rcp_f32_e32 v133, v0
	v_mul_f32_e32 v0, 0x3d372713, v122
	v_mul_f32_e32 v0, v122, v0
	v_fma_f32 v0, v122, v0, v122
	v_mul_f32_e32 v0, 0x3fcc422a, v0
	v_mul_f32_e32 v0, 0xbfb8aa3b, v0
	v_exp_f32_e32 v0, v0
	v_pk_mul_f32 v[128:129], v[128:129], v[132:133]
	v_add_f32_e32 v0, 1.0, v0
	v_rcp_f32_e32 v132, v0
	v_mul_f32_e32 v0, 0x3d372713, v123
	v_mul_f32_e32 v0, v123, v0
	v_fma_f32 v0, v123, v0, v123
	v_mul_f32_e32 v0, 0x3fcc422a, v0
	v_mul_f32_e32 v0, 0xbfb8aa3b, v0
	v_exp_f32_e32 v0, v0
	s_nop 0
	v_add_f32_e32 v0, 1.0, v0
	v_rcp_f32_e32 v133, v0
	s_nop 0
	v_pk_mul_f32 v[132:133], v[122:123], v[132:133]
	v_pk_add_f32 v[122:123], v[124:125], v[48:49]
	s_nop 0
	v_mul_f32_e32 v0, 0x3d372713, v122
	v_mul_f32_e32 v0, v122, v0
	v_fma_f32 v0, v122, v0, v122
	v_mul_f32_e32 v0, 0x3fcc422a, v0
	v_mul_f32_e32 v0, 0xbfb8aa3b, v0
	v_exp_f32_e32 v0, v0
	s_nop 0
	v_add_f32_e32 v0, 1.0, v0
	v_rcp_f32_e32 v124, v0
	v_mul_f32_e32 v0, 0x3d372713, v123
	v_mul_f32_e32 v0, v123, v0
	v_fma_f32 v0, v123, v0, v123
	v_mul_f32_e32 v0, 0x3fcc422a, v0
	v_mul_f32_e32 v0, 0xbfb8aa3b, v0
	v_exp_f32_e32 v0, v0
	s_nop 0
; __device__ __forceinline__ unsigned pk2(float lo, float hi) { const f32x2 f = {lo, hi}; const bf16n2 v = __builtin_convertvector(f, bf16n2); return __builtin_bit_cast(unsigned, v); }
; __device__ __forceinline__ float sigmoidf_(float x) { return __builtin_amdgcn_rcpf(1.0f + __expf(-x)); }
;     __device__ __forceinline__ bool operator()(f32x4 (&acc)[2][2][4][2], const Unit& u, int wr, int wc, int fr, int fq) const {
;     ...
;         for (int ai = 0; ai < 2; ++ai)
; #pragma unroll
;             for (int m = 0; m < 4; ++m) { bf16_t* rowp = hid + ((size_t)kv * 2048 + row0 + ai * HALF + m * 16) * 256 + col0;
; #pragma unroll
;                 for (int bj = 0; bj < 2; ++bj) { float o[8];
; #pragma unroll
;                     for (int j = 0; j < 8; ++j) { const float x = acc[ai][bj][m][j >> 2][j & 3] + bv[bj][j];
;                         o[j] = x * sigmoidf_(1.5957691216f * (x + 0.044715f * x * x * x)); }
;                     u32x4 w; w.x = pk2(o[0], o[1]); w.y = pk2(o[2], o[3]); w.z = pk2(o[4], o[5]); w.w = pk2(o[6], o[7]);
;                     *(u32x4*)(rowp + bj * HALF) = w; } }
	v_add_f32_e32 v0, 1.0, v0
	v_rcp_f32_e32 v125, v0
	v_mul_f32_e32 v0, 0x3d372713, v118
	v_mul_f32_e32 v0, v118, v0
	v_fma_f32 v0, v118, v0, v118
	v_mul_f32_e32 v0, 0x3fcc422a, v0
	v_mul_f32_e32 v0, 0xbfb8aa3b, v0
	v_exp_f32_e32 v0, v0
	v_pk_mul_f32 v[134:135], v[122:123], v[124:125]
	v_cvt_pk_bf16_f32 v122, v126, v127
	v_cvt_pk_bf16_f32 v123, v128, v129
	v_cvt_pk_bf16_f32 v124, v132, v133
	v_cvt_pk_bf16_f32 v125, v134, v135
	v_add_f32_e32 v0, 1.0, v0
	global_store_dwordx4 v[130:131], v[122:125], off
	s_nop 1
	v_rcp_f32_e32 v122, v0
	v_mul_f32_e32 v0, 0x3d372713, v119
	v_mul_f32_e32 v0, v119, v0
	v_fma_f32 v0, v119, v0, v119
	v_mul_f32_e32 v0, 0x3fcc422a, v0
	v_mul_f32_e32 v0, 0xbfb8aa3b, v0
	v_exp_f32_e32 v0, v0
	s_nop 0
	v_add_f32_e32 v0, 1.0, v0
	v_rcp_f32_e32 v123, v0
	v_mul_f32_e32 v0, 0x3d372713, v120
	v_mul_f32_e32 v0, v120, v0
	v_fma_f32 v0, v120, v0, v120
	v_mul_f32_e32 v0, 0x3fcc422a, v0
	v_mul_f32_e32 v0, 0xbfb8aa3b, v0
	v_exp_f32_e32 v0, v0
	v_pk_mul_f32 v[118:119], v[118:119], v[122:123]
	v_add_f32_e32 v0, 1.0, v0
	v_rcp_f32_e32 v122, v0
	v_mul_f32_e32 v0, 0x3d372713, v121
	v_mul_f32_e32 v0, v121, v0
	v_fma_f32 v0, v121, v0, v121
	v_mul_f32_e32 v0, 0x3fcc422a, v0
	v_mul_f32_e32 v0, 0xbfb8aa3b, v0
	v_exp_f32_e32 v0, v0
	s_nop 0
	v_add_f32_e32 v0, 1.0, v0
	v_rcp_f32_e32 v123, v0
	v_mul_f32_e32 v0, 0x3d372713, v114
	v_mul_f32_e32 v0, v114, v0
	v_fma_f32 v0, v114, v0, v114
	v_mul_f32_e32 v0, 0x3fcc422a, v0
	v_mul_f32_e32 v0, 0xbfb8aa3b, v0
	v_exp_f32_e32 v0, v0
	v_pk_mul_f32 v[120:121], v[120:121], v[122:123]
	v_add_f32_e32 v0, 1.0, v0
	v_rcp_f32_e32 v122, v0
	v_mul_f32_e32 v0, 0x3d372713, v115
	v_mul_f32_e32 v0, v115, v0
	v_fma_f32 v0, v115, v0, v115
	v_mul_f32_e32 v0, 0x3fcc422a, v0
	v_mul_f32_e32 v0, 0xbfb8aa3b, v0
	v_exp_f32_e32 v0, v0
	s_nop 0
	v_add_f32_e32 v0, 1.0, v0
	v_rcp_f32_e32 v123, v0
	s_nop 0
	v_pk_mul_f32 v[122:123], v[114:115], v[122:123]
	v_pk_add_f32 v[114:115], v[116:117], v[40:41]
	s_nop 0
	v_mul_f32_e32 v0, 0x3d372713, v114
	v_mul_f32_e32 v0, v114, v0
	v_fma_f32 v0, v114, v0, v114
	v_mul_f32_e32 v0, 0x3fcc422a, v0
	v_mul_f32_e32 v0, 0xbfb8aa3b, v0
	v_exp_f32_e32 v0, v0
	s_nop 0
	v_add_f32_e32 v0, 1.0, v0
	v_rcp_f32_e32 v116, v0
	v_mul_f32_e32 v0, 0x3d372713, v115
	v_mul_f32_e32 v0, v115, v0
	v_fma_f32 v0, v115, v0, v115
	v_mul_f32_e32 v0, 0x3fcc422a, v0
	v_mul_f32_e32 v0, 0xbfb8aa3b, v0
	v_exp_f32_e32 v0, v0
	s_nop 0
	v_add_f32_e32 v0, 1.0, v0
	v_rcp_f32_e32 v117, v0
	v_mul_f32_e32 v0, 0x3d372713, v110
	v_mul_f32_e32 v0, v110, v0
	v_fma_f32 v0, v110, v0, v110
	v_mul_f32_e32 v0, 0x3fcc422a, v0
	v_mul_f32_e32 v0, 0xbfb8aa3b, v0
	v_exp_f32_e32 v0, v0
	v_pk_mul_f32 v[124:125], v[114:115], v[116:117]
	v_cvt_pk_bf16_f32 v114, v118, v119
	v_cvt_pk_bf16_f32 v115, v120, v121
	v_cvt_pk_bf16_f32 v116, v122, v123
	v_cvt_pk_bf16_f32 v117, v124, v125
	v_add_f32_e32 v0, 1.0, v0
	global_store_dwordx4 v[130:131], v[114:117], off offset:256
	s_nop 1
	v_rcp_f32_e32 v116, v0
	v_mul_f32_e32 v0, 0x3d372713, v111
	v_mul_f32_e32 v0, v111, v0
	v_fma_f32 v0, v111, v0, v111
	v_mul_f32_e32 v0, 0x3fcc422a, v0
	v_mul_f32_e32 v0, 0xbfb8aa3b, v0
	v_exp_f32_e32 v0, v0
	v_or_b32_e32 v114, 0x4000, v160
	v_mov_b32_e32 v115, v161
	v_lshl_add_u64 v[114:115], v[152:153], 0, v[114:115]
	v_add_f32_e32 v0, 1.0, v0
	v_rcp_f32_e32 v117, v0
	v_mul_f32_e32 v0, 0x3d372713, v112
	v_mul_f32_e32 v0, v112, v0
	v_fma_f32 v0, v112, v0, v112
	v_mul_f32_e32 v0, 0x3fcc422a, v0
	v_mul_f32_e32 v0, 0xbfb8aa3b, v0
	v_exp_f32_e32 v0, v0
	v_pk_mul_f32 v[110:111], v[110:111], v[116:117]
	v_or_b32_e32 v160, 0x6000, v160
	v_add_f32_e32 v0, 1.0, v0
	v_rcp_f32_e32 v116, v0
	v_mul_f32_e32 v0, 0x3d372713, v113
	v_mul_f32_e32 v0, v113, v0
	v_fma_f32 v0, v113, v0, v113
	v_mul_f32_e32 v0, 0x3fcc422a, v0
	v_mul_f32_e32 v0, 0xbfb8aa3b, v0
	v_exp_f32_e32 v0, v0
	s_nop 0
	v_add_f32_e32 v0, 1.0, v0
	v_rcp_f32_e32 v117, v0
	v_mul_f32_e32 v0, 0x3d372713, v106
	v_mul_f32_e32 v0, v106, v0
	v_fma_f32 v0, v106, v0, v106
	v_mul_f32_e32 v0, 0x3fcc422a, v0
	v_mul_f32_e32 v0, 0xbfb8aa3b, v0
	v_exp_f32_e32 v0, v0
	v_pk_mul_f32 v[112:113], v[112:113], v[116:117]
	v_add_f32_e32 v0, 1.0, v0
	v_rcp_f32_e32 v116, v0
	v_mul_f32_e32 v0, 0x3d372713, v107
	v_mul_f32_e32 v0, v107, v0
	v_fma_f32 v0, v107, v0, v107
	v_mul_f32_e32 v0, 0x3fcc422a, v0
	v_mul_f32_e32 v0, 0xbfb8aa3b, v0
	v_exp_f32_e32 v0, v0
	s_nop 0
	v_add_f32_e32 v0, 1.0, v0
	v_rcp_f32_e32 v117, v0
	s_nop 0
	v_pk_mul_f32 v[116:117], v[106:107], v[116:117]
	v_pk_add_f32 v[106:107], v[108:109], v[48:49]
	s_nop 0
	v_mul_f32_e32 v0, 0x3d372713, v106
	v_mul_f32_e32 v0, v106, v0
	v_fma_f32 v0, v106, v0, v106
	v_mul_f32_e32 v0, 0x3fcc422a, v0
	v_mul_f32_e32 v0, 0xbfb8aa3b, v0
	v_exp_f32_e32 v0, v0
	s_nop 0
	v_add_f32_e32 v0, 1.0, v0
	v_rcp_f32_e32 v108, v0
	v_mul_f32_e32 v0, 0x3d372713, v107
	v_mul_f32_e32 v0, v107, v0
	v_fma_f32 v0, v107, v0, v107
	v_mul_f32_e32 v0, 0x3fcc422a, v0
	v_mul_f32_e32 v0, 0xbfb8aa3b, v0
	v_exp_f32_e32 v0, v0
	s_nop 0
	v_add_f32_e32 v0, 1.0, v0
	v_rcp_f32_e32 v109, v0
	v_mul_f32_e32 v0, 0x3d372713, v102
	v_mul_f32_e32 v0, v102, v0
	v_fma_f32 v0, v102, v0, v102
	v_mul_f32_e32 v0, 0x3fcc422a, v0
	v_mul_f32_e32 v0, 0xbfb8aa3b, v0
	v_exp_f32_e32 v0, v0
	v_pk_mul_f32 v[118:119], v[106:107], v[108:109]
	v_cvt_pk_bf16_f32 v106, v110, v111
	v_cvt_pk_bf16_f32 v107, v112, v113
	v_cvt_pk_bf16_f32 v108, v116, v117
	v_cvt_pk_bf16_f32 v109, v118, v119
	v_add_f32_e32 v0, 1.0, v0
	global_store_dwordx4 v[114:115], v[106:109], off
	s_nop 1
	v_rcp_f32_e32 v106, v0
	v_mul_f32_e32 v0, 0x3d372713, v103
	v_mul_f32_e32 v0, v103, v0
	v_fma_f32 v0, v103, v0, v103
	v_mul_f32_e32 v0, 0x3fcc422a, v0
	v_mul_f32_e32 v0, 0xbfb8aa3b, v0
	v_exp_f32_e32 v0, v0
; __device__ __forceinline__ unsigned pk2(float lo, float hi) { const f32x2 f = {lo, hi}; const bf16n2 v = __builtin_convertvector(f, bf16n2); return __builtin_bit_cast(unsigned, v); }
; __device__ __forceinline__ float sigmoidf_(float x) { return __builtin_amdgcn_rcpf(1.0f + __expf(-x)); }
;     __device__ __forceinline__ bool operator()(f32x4 (&acc)[2][2][4][2], const Unit& u, int wr, int wc, int fr, int fq) const {
;     ...
;         for (int ai = 0; ai < 2; ++ai)
; #pragma unroll
;             for (int m = 0; m < 4; ++m) { bf16_t* rowp = hid + ((size_t)kv * 2048 + row0 + ai * HALF + m * 16) * 256 + col0;
; #pragma unroll
;                 for (int bj = 0; bj < 2; ++bj) { float o[8];
; #pragma unroll
;                     for (int j = 0; j < 8; ++j) { const float x = acc[ai][bj][m][j >> 2][j & 3] + bv[bj][j];
;                         o[j] = x * sigmoidf_(1.5957691216f * (x + 0.044715f * x * x * x)); }
;                     u32x4 w; w.x = pk2(o[0], o[1]); w.y = pk2(o[2], o[3]); w.z = pk2(o[4], o[5]); w.w = pk2(o[6], o[7]);
;                     *(u32x4*)(rowp + bj * HALF) = w; } }
	s_nop 0
	v_add_f32_e32 v0, 1.0, v0
	v_rcp_f32_e32 v107, v0
	v_mul_f32_e32 v0, 0x3d372713, v104
	v_mul_f32_e32 v0, v104, v0
	v_fma_f32 v0, v104, v0, v104
	v_mul_f32_e32 v0, 0x3fcc422a, v0
	v_mul_f32_e32 v0, 0xbfb8aa3b, v0
	v_exp_f32_e32 v0, v0
	v_pk_mul_f32 v[102:103], v[102:103], v[106:107]
	v_add_f32_e32 v0, 1.0, v0
	v_rcp_f32_e32 v106, v0
	v_mul_f32_e32 v0, 0x3d372713, v105
	v_mul_f32_e32 v0, v105, v0
	v_fma_f32 v0, v105, v0, v105
	v_mul_f32_e32 v0, 0x3fcc422a, v0
	v_mul_f32_e32 v0, 0xbfb8aa3b, v0
	v_exp_f32_e32 v0, v0
	s_nop 0
	v_add_f32_e32 v0, 1.0, v0
	v_rcp_f32_e32 v107, v0
	v_mul_f32_e32 v0, 0x3d372713, v98
	v_mul_f32_e32 v0, v98, v0
	v_fma_f32 v0, v98, v0, v98
	v_mul_f32_e32 v0, 0x3fcc422a, v0
	v_mul_f32_e32 v0, 0xbfb8aa3b, v0
	v_exp_f32_e32 v0, v0
	v_pk_mul_f32 v[104:105], v[104:105], v[106:107]
	v_add_f32_e32 v0, 1.0, v0
	v_rcp_f32_e32 v106, v0
	v_mul_f32_e32 v0, 0x3d372713, v99
	v_mul_f32_e32 v0, v99, v0
	v_fma_f32 v0, v99, v0, v99
	v_mul_f32_e32 v0, 0x3fcc422a, v0
	v_mul_f32_e32 v0, 0xbfb8aa3b, v0
	v_exp_f32_e32 v0, v0
	s_nop 0
	v_add_f32_e32 v0, 1.0, v0
	v_rcp_f32_e32 v107, v0
	s_nop 0
	v_pk_mul_f32 v[106:107], v[98:99], v[106:107]
	v_pk_add_f32 v[98:99], v[100:101], v[40:41]
	s_nop 0
	v_mul_f32_e32 v0, 0x3d372713, v98
	v_mul_f32_e32 v0, v98, v0
	v_fma_f32 v0, v98, v0, v98
	v_mul_f32_e32 v0, 0x3fcc422a, v0
	v_mul_f32_e32 v0, 0xbfb8aa3b, v0
	v_exp_f32_e32 v0, v0
	s_nop 0
	v_add_f32_e32 v0, 1.0, v0
	v_rcp_f32_e32 v100, v0
	v_mul_f32_e32 v0, 0x3d372713, v99
	v_mul_f32_e32 v0, v99, v0
	v_fma_f32 v0, v99, v0, v99
	v_mul_f32_e32 v0, 0x3fcc422a, v0
	v_mul_f32_e32 v0, 0xbfb8aa3b, v0
	v_exp_f32_e32 v0, v0
	s_nop 0
	v_add_f32_e32 v0, 1.0, v0
	v_rcp_f32_e32 v101, v0
	v_mul_f32_e32 v0, 0x3d372713, v94
	v_mul_f32_e32 v0, v94, v0
	v_fma_f32 v0, v94, v0, v94
	v_mul_f32_e32 v0, 0x3fcc422a, v0
	v_mul_f32_e32 v0, 0xbfb8aa3b, v0
	v_exp_f32_e32 v0, v0
	v_pk_mul_f32 v[108:109], v[98:99], v[100:101]
	v_cvt_pk_bf16_f32 v98, v102, v103
	v_cvt_pk_bf16_f32 v99, v104, v105
	v_cvt_pk_bf16_f32 v100, v106, v107
	v_cvt_pk_bf16_f32 v101, v108, v109
	v_add_f32_e32 v0, 1.0, v0
	global_store_dwordx4 v[114:115], v[98:101], off offset:256
	s_nop 1
	v_rcp_f32_e32 v100, v0
	v_mul_f32_e32 v0, 0x3d372713, v95
	v_mul_f32_e32 v0, v95, v0
	v_fma_f32 v0, v95, v0, v95
	v_mul_f32_e32 v0, 0x3fcc422a, v0
	v_mul_f32_e32 v0, 0xbfb8aa3b, v0
	v_exp_f32_e32 v0, v0
	v_lshl_add_u64 v[98:99], v[152:153], 0, v[160:161]
	v_add_f32_e32 v0, 1.0, v0
	v_rcp_f32_e32 v101, v0
	v_mul_f32_e32 v0, 0x3d372713, v96
	v_mul_f32_e32 v0, v96, v0
	v_fma_f32 v0, v96, v0, v96
	v_mul_f32_e32 v0, 0x3fcc422a, v0
	v_mul_f32_e32 v0, 0xbfb8aa3b, v0
	v_exp_f32_e32 v0, v0
	v_pk_mul_f32 v[94:95], v[94:95], v[100:101]
	v_add_f32_e32 v0, 1.0, v0
	v_rcp_f32_e32 v100, v0
	v_mul_f32_e32 v0, 0x3d372713, v97
	v_mul_f32_e32 v0, v97, v0
	v_fma_f32 v0, v97, v0, v97
	v_mul_f32_e32 v0, 0x3fcc422a, v0
	v_mul_f32_e32 v0, 0xbfb8aa3b, v0
	v_exp_f32_e32 v0, v0
	s_nop 0
	v_add_f32_e32 v0, 1.0, v0
	v_rcp_f32_e32 v101, v0
	v_mul_f32_e32 v0, 0x3d372713, v90
	v_mul_f32_e32 v0, v90, v0
	v_fma_f32 v0, v90, v0, v90
	v_mul_f32_e32 v0, 0x3fcc422a, v0
	v_mul_f32_e32 v0, 0xbfb8aa3b, v0
	v_exp_f32_e32 v0, v0
	v_pk_mul_f32 v[96:97], v[96:97], v[100:101]
	v_add_f32_e32 v0, 1.0, v0
	v_rcp_f32_e32 v100, v0
	v_mul_f32_e32 v0, 0x3d372713, v91
	v_mul_f32_e32 v0, v91, v0
	v_fma_f32 v0, v91, v0, v91
	v_mul_f32_e32 v0, 0x3fcc422a, v0
	v_mul_f32_e32 v0, 0xbfb8aa3b, v0
	v_exp_f32_e32 v0, v0
	s_nop 0
	v_add_f32_e32 v0, 1.0, v0
	v_rcp_f32_e32 v101, v0
	s_nop 0
	v_pk_mul_f32 v[100:101], v[90:91], v[100:101]
	v_pk_add_f32 v[90:91], v[92:93], v[48:49]
	s_nop 0
	v_mul_f32_e32 v0, 0x3d372713, v90
	v_mul_f32_e32 v0, v90, v0
	v_fma_f32 v0, v90, v0, v90
	v_mul_f32_e32 v0, 0x3fcc422a, v0
	v_mul_f32_e32 v0, 0xbfb8aa3b, v0
	v_exp_f32_e32 v0, v0
	s_nop 0
	v_add_f32_e32 v0, 1.0, v0
	v_rcp_f32_e32 v92, v0
	v_mul_f32_e32 v0, 0x3d372713, v91
	v_mul_f32_e32 v0, v91, v0
	v_fma_f32 v0, v91, v0, v91
	v_mul_f32_e32 v0, 0x3fcc422a, v0
	v_mul_f32_e32 v0, 0xbfb8aa3b, v0
	v_exp_f32_e32 v0, v0
	s_nop 0
	v_add_f32_e32 v0, 1.0, v0
	v_rcp_f32_e32 v93, v0
	v_mul_f32_e32 v0, 0x3d372713, v86
	v_mul_f32_e32 v0, v86, v0
	v_fma_f32 v0, v86, v0, v86
	v_mul_f32_e32 v0, 0x3fcc422a, v0
	v_mul_f32_e32 v0, 0xbfb8aa3b, v0
	v_exp_f32_e32 v0, v0
	v_pk_mul_f32 v[102:103], v[90:91], v[92:93]
	v_cvt_pk_bf16_f32 v90, v94, v95
	v_cvt_pk_bf16_f32 v91, v96, v97
	v_cvt_pk_bf16_f32 v92, v100, v101
	v_cvt_pk_bf16_f32 v93, v102, v103
	v_add_f32_e32 v0, 1.0, v0
	global_store_dwordx4 v[98:99], v[90:93], off
	s_nop 1
	v_rcp_f32_e32 v90, v0
	v_mul_f32_e32 v0, 0x3d372713, v87
	v_mul_f32_e32 v0, v87, v0
	v_fma_f32 v0, v87, v0, v87
	v_mul_f32_e32 v0, 0x3fcc422a, v0
	v_mul_f32_e32 v0, 0xbfb8aa3b, v0
	v_exp_f32_e32 v0, v0
	s_nop 0
	v_add_f32_e32 v0, 1.0, v0
	v_rcp_f32_e32 v91, v0
	v_mul_f32_e32 v0, 0x3d372713, v88
	v_mul_f32_e32 v0, v88, v0
	v_fma_f32 v0, v88, v0, v88
	v_mul_f32_e32 v0, 0x3fcc422a, v0
	v_mul_f32_e32 v0, 0xbfb8aa3b, v0
	v_exp_f32_e32 v0, v0
	v_pk_mul_f32 v[86:87], v[86:87], v[90:91]
	v_add_f32_e32 v0, 1.0, v0
	v_rcp_f32_e32 v90, v0
	v_mul_f32_e32 v0, 0x3d372713, v89
	v_mul_f32_e32 v0, v89, v0
	v_fma_f32 v0, v89, v0, v89
	v_mul_f32_e32 v0, 0x3fcc422a, v0
	v_mul_f32_e32 v0, 0xbfb8aa3b, v0
	v_exp_f32_e32 v0, v0
	s_nop 0
	v_add_f32_e32 v0, 1.0, v0
	v_rcp_f32_e32 v91, v0
	v_mul_f32_e32 v0, 0x3d372713, v82
	v_mul_f32_e32 v0, v82, v0
	v_fma_f32 v0, v82, v0, v82
	v_mul_f32_e32 v0, 0x3fcc422a, v0
	v_mul_f32_e32 v0, 0xbfb8aa3b, v0
	v_exp_f32_e32 v0, v0
	v_pk_mul_f32 v[88:89], v[88:89], v[90:91]
	v_add_f32_e32 v0, 1.0, v0
	v_rcp_f32_e32 v90, v0
	v_mul_f32_e32 v0, 0x3d372713, v83
	v_mul_f32_e32 v0, v83, v0
; __device__ __forceinline__ unsigned pk2(float lo, float hi) { const f32x2 f = {lo, hi}; const bf16n2 v = __builtin_convertvector(f, bf16n2); return __builtin_bit_cast(unsigned, v); }
; __device__ __forceinline__ float sigmoidf_(float x) { return __builtin_amdgcn_rcpf(1.0f + __expf(-x)); }
;     __device__ __forceinline__ bool operator()(f32x4 (&acc)[2][2][4][2], const Unit& u, int wr, int wc, int fr, int fq) const {
;     ...
;         for (int ai = 0; ai < 2; ++ai)
; #pragma unroll
;             for (int m = 0; m < 4; ++m) { bf16_t* rowp = hid + ((size_t)kv * 2048 + row0 + ai * HALF + m * 16) * 256 + col0;
; #pragma unroll
;                 for (int bj = 0; bj < 2; ++bj) { float o[8];
; #pragma unroll
;                     for (int j = 0; j < 8; ++j) { const float x = acc[ai][bj][m][j >> 2][j & 3] + bv[bj][j];
;                         o[j] = x * sigmoidf_(1.5957691216f * (x + 0.044715f * x * x * x)); }
;                     u32x4 w; w.x = pk2(o[0], o[1]); w.y = pk2(o[2], o[3]); w.z = pk2(o[4], o[5]); w.w = pk2(o[6], o[7]);
;                     *(u32x4*)(rowp + bj * HALF) = w; } }
	v_fma_f32 v0, v83, v0, v83
	v_mul_f32_e32 v0, 0x3fcc422a, v0
	v_mul_f32_e32 v0, 0xbfb8aa3b, v0
	v_exp_f32_e32 v0, v0
	s_nop 0
	v_add_f32_e32 v0, 1.0, v0
	v_rcp_f32_e32 v91, v0
	s_nop 0
	v_pk_mul_f32 v[90:91], v[82:83], v[90:91]
	v_pk_add_f32 v[82:83], v[84:85], v[40:41]
	s_nop 0
	v_mul_f32_e32 v0, 0x3d372713, v82
	v_mul_f32_e32 v0, v82, v0
	v_fma_f32 v0, v82, v0, v82
	v_mul_f32_e32 v0, 0x3fcc422a, v0
	v_mul_f32_e32 v0, 0xbfb8aa3b, v0
	v_exp_f32_e32 v0, v0
	s_nop 0
	v_add_f32_e32 v0, 1.0, v0
	v_rcp_f32_e32 v84, v0
	v_mul_f32_e32 v0, 0x3d372713, v83
	v_mul_f32_e32 v0, v83, v0
	v_fma_f32 v0, v83, v0, v83
	v_mul_f32_e32 v0, 0x3fcc422a, v0
	v_mul_f32_e32 v0, 0xbfb8aa3b, v0
	v_exp_f32_e32 v0, v0
	s_nop 0
	v_add_f32_e32 v0, 1.0, v0
	v_rcp_f32_e32 v85, v0
	v_mul_f32_e32 v0, 0x3d372713, v78
	v_mul_f32_e32 v0, v78, v0
	v_fma_f32 v0, v78, v0, v78
	v_mul_f32_e32 v0, 0x3fcc422a, v0
	v_mul_f32_e32 v0, 0xbfb8aa3b, v0
	v_exp_f32_e32 v0, v0
	v_pk_mul_f32 v[92:93], v[82:83], v[84:85]
	v_cvt_pk_bf16_f32 v82, v86, v87
	v_cvt_pk_bf16_f32 v83, v88, v89
	v_cvt_pk_bf16_f32 v84, v90, v91
	v_cvt_pk_bf16_f32 v85, v92, v93
	v_add_f32_e32 v0, 1.0, v0
	global_store_dwordx4 v[98:99], v[82:85], off offset:256
	s_nop 1
	v_rcp_f32_e32 v84, v0
	v_mul_f32_e32 v0, 0x3d372713, v79
	v_mul_f32_e32 v0, v79, v0
	v_fma_f32 v0, v79, v0, v79
	v_mul_f32_e32 v0, 0x3fcc422a, v0
	v_mul_f32_e32 v0, 0xbfb8aa3b, v0
	v_exp_f32_e32 v0, v0
	v_lshl_add_u64 v[82:83], v[158:159], 0, s[6:7]
	s_mov_b32 s6, 0x10000
	v_add_f32_e32 v0, 1.0, v0
	v_rcp_f32_e32 v85, v0
	v_mul_f32_e32 v0, 0x3d372713, v80
	v_mul_f32_e32 v0, v80, v0
	v_fma_f32 v0, v80, v0, v80
	v_mul_f32_e32 v0, 0x3fcc422a, v0
	v_mul_f32_e32 v0, 0xbfb8aa3b, v0
	v_exp_f32_e32 v0, v0
	v_pk_mul_f32 v[78:79], v[78:79], v[84:85]
	v_add_f32_e32 v0, 1.0, v0
	v_rcp_f32_e32 v84, v0
	v_mul_f32_e32 v0, 0x3d372713, v81
	v_mul_f32_e32 v0, v81, v0
	v_fma_f32 v0, v81, v0, v81
	v_mul_f32_e32 v0, 0x3fcc422a, v0
	v_mul_f32_e32 v0, 0xbfb8aa3b, v0
	v_exp_f32_e32 v0, v0
	s_nop 0
	v_add_f32_e32 v0, 1.0, v0
	v_rcp_f32_e32 v85, v0
	v_mul_f32_e32 v0, 0x3d372713, v74
	v_mul_f32_e32 v0, v74, v0
	v_fma_f32 v0, v74, v0, v74
	v_mul_f32_e32 v0, 0x3fcc422a, v0
	v_mul_f32_e32 v0, 0xbfb8aa3b, v0
	v_exp_f32_e32 v0, v0
	v_pk_mul_f32 v[80:81], v[80:81], v[84:85]
	v_add_f32_e32 v0, 1.0, v0
	v_rcp_f32_e32 v84, v0
	v_mul_f32_e32 v0, 0x3d372713, v75
	v_mul_f32_e32 v0, v75, v0
	v_fma_f32 v0, v75, v0, v75
	v_mul_f32_e32 v0, 0x3fcc422a, v0
	v_mul_f32_e32 v0, 0xbfb8aa3b, v0
	v_exp_f32_e32 v0, v0
	s_nop 0
	v_add_f32_e32 v0, 1.0, v0
	v_rcp_f32_e32 v85, v0
	s_nop 0
	v_pk_mul_f32 v[84:85], v[74:75], v[84:85]
	v_pk_add_f32 v[74:75], v[76:77], v[48:49]
	s_nop 0
	v_mul_f32_e32 v0, 0x3d372713, v74
	v_mul_f32_e32 v0, v74, v0
	v_fma_f32 v0, v74, v0, v74
	v_mul_f32_e32 v0, 0x3fcc422a, v0
	v_mul_f32_e32 v0, 0xbfb8aa3b, v0
	v_exp_f32_e32 v0, v0
	s_nop 0
	v_add_f32_e32 v0, 1.0, v0
	v_rcp_f32_e32 v76, v0
	v_mul_f32_e32 v0, 0x3d372713, v75
	v_mul_f32_e32 v0, v75, v0
	v_fma_f32 v0, v75, v0, v75
	v_mul_f32_e32 v0, 0x3fcc422a, v0
	v_mul_f32_e32 v0, 0xbfb8aa3b, v0
	v_exp_f32_e32 v0, v0
	s_nop 0
	v_add_f32_e32 v0, 1.0, v0
	v_rcp_f32_e32 v77, v0
	v_mul_f32_e32 v0, 0x3d372713, v70
	v_mul_f32_e32 v0, v70, v0
	v_fma_f32 v0, v70, v0, v70
	v_mul_f32_e32 v0, 0x3fcc422a, v0
	v_mul_f32_e32 v0, 0xbfb8aa3b, v0
	v_exp_f32_e32 v0, v0
	v_pk_mul_f32 v[86:87], v[74:75], v[76:77]
	v_cvt_pk_bf16_f32 v74, v78, v79
	v_add_co_u32_e32 v78, vcc, s6, v158
	v_cvt_pk_bf16_f32 v75, v80, v81
	v_cvt_pk_bf16_f32 v76, v84, v85
	v_cvt_pk_bf16_f32 v77, v86, v87
	v_addc_co_u32_e32 v79, vcc, 0, v159, vcc
	v_add_f32_e32 v0, 1.0, v0
	global_store_dwordx4 v[78:79], v[74:77], off
	s_mov_b64 s[6:7], 0x12000
	s_nop 0
	v_rcp_f32_e32 v74, v0
	v_mul_f32_e32 v0, 0x3d372713, v71
	v_mul_f32_e32 v0, v71, v0
	v_fma_f32 v0, v71, v0, v71
	v_mul_f32_e32 v0, 0x3fcc422a, v0
	v_mul_f32_e32 v0, 0xbfb8aa3b, v0
	v_exp_f32_e32 v0, v0
	s_nop 0
	v_add_f32_e32 v0, 1.0, v0
	v_rcp_f32_e32 v75, v0
	v_mul_f32_e32 v0, 0x3d372713, v72
	v_mul_f32_e32 v0, v72, v0
	v_fma_f32 v0, v72, v0, v72
	v_mul_f32_e32 v0, 0x3fcc422a, v0
	v_mul_f32_e32 v0, 0xbfb8aa3b, v0
	v_exp_f32_e32 v0, v0
	v_pk_mul_f32 v[70:71], v[70:71], v[74:75]
	v_add_f32_e32 v0, 1.0, v0
	v_rcp_f32_e32 v74, v0
	v_mul_f32_e32 v0, 0x3d372713, v73
	v_mul_f32_e32 v0, v73, v0
	v_fma_f32 v0, v73, v0, v73
	v_mul_f32_e32 v0, 0x3fcc422a, v0
	v_mul_f32_e32 v0, 0xbfb8aa3b, v0
	v_exp_f32_e32 v0, v0
	s_nop 0
	v_add_f32_e32 v0, 1.0, v0
	v_rcp_f32_e32 v75, v0
	v_mul_f32_e32 v0, 0x3d372713, v62
	v_mul_f32_e32 v0, v62, v0
	v_fma_f32 v0, v62, v0, v62
	v_mul_f32_e32 v0, 0x3fcc422a, v0
	v_mul_f32_e32 v0, 0xbfb8aa3b, v0
	v_exp_f32_e32 v0, v0
	v_pk_mul_f32 v[72:73], v[72:73], v[74:75]
	v_add_f32_e32 v0, 1.0, v0
	v_rcp_f32_e32 v74, v0
	v_mul_f32_e32 v0, 0x3d372713, v63
	v_mul_f32_e32 v0, v63, v0
	v_fma_f32 v0, v63, v0, v63
	v_mul_f32_e32 v0, 0x3fcc422a, v0
	v_mul_f32_e32 v0, 0xbfb8aa3b, v0
	v_exp_f32_e32 v0, v0
	s_nop 0
	v_add_f32_e32 v0, 1.0, v0
	v_rcp_f32_e32 v75, v0
	s_nop 0
	v_pk_mul_f32 v[74:75], v[62:63], v[74:75]
	v_pk_add_f32 v[62:63], v[64:65], v[40:41]
	s_nop 0
	v_mul_f32_e32 v0, 0x3d372713, v62
	v_mul_f32_e32 v0, v62, v0
	v_fma_f32 v0, v62, v0, v62
	v_mul_f32_e32 v0, 0x3fcc422a, v0
	v_mul_f32_e32 v0, 0xbfb8aa3b, v0
	v_exp_f32_e32 v0, v0
	s_nop 0
	v_add_f32_e32 v0, 1.0, v0
	v_rcp_f32_e32 v64, v0
	v_mul_f32_e32 v0, 0x3d372713, v63
	v_mul_f32_e32 v0, v63, v0
	v_fma_f32 v0, v63, v0, v63
	v_mul_f32_e32 v0, 0x3fcc422a, v0
	v_mul_f32_e32 v0, 0xbfb8aa3b, v0
	v_exp_f32_e32 v0, v0
	s_nop 0
	v_add_f32_e32 v0, 1.0, v0
	v_rcp_f32_e32 v65, v0
	v_mul_f32_e32 v0, 0x3d372713, v58
	v_mul_f32_e32 v0, v58, v0
	v_fma_f32 v0, v58, v0, v58
; __device__ __forceinline__ unsigned pk2(float lo, float hi) { const f32x2 f = {lo, hi}; const bf16n2 v = __builtin_convertvector(f, bf16n2); return __builtin_bit_cast(unsigned, v); }
; __device__ __forceinline__ float sigmoidf_(float x) { return __builtin_amdgcn_rcpf(1.0f + __expf(-x)); }
;     __device__ __forceinline__ bool operator()(f32x4 (&acc)[2][2][4][2], const Unit& u, int wr, int wc, int fr, int fq) const {
;     ...
;         for (int ai = 0; ai < 2; ++ai)
; #pragma unroll
;             for (int m = 0; m < 4; ++m) { bf16_t* rowp = hid + ((size_t)kv * 2048 + row0 + ai * HALF + m * 16) * 256 + col0;
; #pragma unroll
;                 for (int bj = 0; bj < 2; ++bj) { float o[8];
; #pragma unroll
;                     for (int j = 0; j < 8; ++j) { const float x = acc[ai][bj][m][j >> 2][j & 3] + bv[bj][j];
;                         o[j] = x * sigmoidf_(1.5957691216f * (x + 0.044715f * x * x * x)); }
;                     u32x4 w; w.x = pk2(o[0], o[1]); w.y = pk2(o[2], o[3]); w.z = pk2(o[4], o[5]); w.w = pk2(o[6], o[7]);
;                     *(u32x4*)(rowp + bj * HALF) = w; } }
	v_mul_f32_e32 v0, 0x3fcc422a, v0
	v_mul_f32_e32 v0, 0xbfb8aa3b, v0
	v_exp_f32_e32 v0, v0
	v_pk_mul_f32 v[76:77], v[62:63], v[64:65]
	v_cvt_pk_bf16_f32 v62, v70, v71
	v_cvt_pk_bf16_f32 v63, v72, v73
	v_cvt_pk_bf16_f32 v64, v74, v75
	v_cvt_pk_bf16_f32 v65, v76, v77
	v_add_f32_e32 v0, 1.0, v0
	global_store_dwordx4 v[82:83], v[62:65], off offset:256
	s_nop 1
	v_rcp_f32_e32 v64, v0
	v_mul_f32_e32 v0, 0x3d372713, v59
	v_mul_f32_e32 v0, v59, v0
	v_fma_f32 v0, v59, v0, v59
	v_mul_f32_e32 v0, 0x3fcc422a, v0
	v_mul_f32_e32 v0, 0xbfb8aa3b, v0
	v_exp_f32_e32 v0, v0
	v_lshl_add_u64 v[62:63], v[158:159], 0, s[6:7]
	s_mov_b32 s6, 0x12000
	v_add_f32_e32 v0, 1.0, v0
	v_rcp_f32_e32 v65, v0
	v_mul_f32_e32 v0, 0x3d372713, v60
	v_mul_f32_e32 v0, v60, v0
	v_fma_f32 v0, v60, v0, v60
	v_mul_f32_e32 v0, 0x3fcc422a, v0
	v_mul_f32_e32 v0, 0xbfb8aa3b, v0
	v_exp_f32_e32 v0, v0
	v_pk_mul_f32 v[58:59], v[58:59], v[64:65]
	v_add_f32_e32 v0, 1.0, v0
	v_rcp_f32_e32 v64, v0
	v_mul_f32_e32 v0, 0x3d372713, v61
	v_mul_f32_e32 v0, v61, v0
	v_fma_f32 v0, v61, v0, v61
	v_mul_f32_e32 v0, 0x3fcc422a, v0
	v_mul_f32_e32 v0, 0xbfb8aa3b, v0
	v_exp_f32_e32 v0, v0
	s_nop 0
	v_add_f32_e32 v0, 1.0, v0
	v_rcp_f32_e32 v65, v0
	v_mul_f32_e32 v0, 0x3d372713, v50
	v_mul_f32_e32 v0, v50, v0
	v_fma_f32 v0, v50, v0, v50
	v_mul_f32_e32 v0, 0x3fcc422a, v0
	v_mul_f32_e32 v0, 0xbfb8aa3b, v0
	v_exp_f32_e32 v0, v0
	v_pk_mul_f32 v[60:61], v[60:61], v[64:65]
	v_add_f32_e32 v0, 1.0, v0
	v_rcp_f32_e32 v64, v0
	v_mul_f32_e32 v0, 0x3d372713, v51
	v_mul_f32_e32 v0, v51, v0
	v_fma_f32 v0, v51, v0, v51
	v_mul_f32_e32 v0, 0x3fcc422a, v0
	v_mul_f32_e32 v0, 0xbfb8aa3b, v0
	v_exp_f32_e32 v0, v0
	s_nop 0
	v_add_f32_e32 v0, 1.0, v0
	v_rcp_f32_e32 v65, v0
	s_nop 0
	v_pk_mul_f32 v[64:65], v[50:51], v[64:65]
	v_pk_add_f32 v[50:51], v[52:53], v[48:49]
	s_nop 0
	v_mul_f32_e32 v0, 0x3d372713, v50
	v_mul_f32_e32 v0, v50, v0
	v_fma_f32 v0, v50, v0, v50
	v_mul_f32_e32 v0, 0x3fcc422a, v0
	v_mul_f32_e32 v0, 0xbfb8aa3b, v0
	v_exp_f32_e32 v0, v0
	s_nop 0
	v_add_f32_e32 v0, 1.0, v0
	v_rcp_f32_e32 v52, v0
	v_mul_f32_e32 v0, 0x3d372713, v51
	v_mul_f32_e32 v0, v51, v0
	v_fma_f32 v0, v51, v0, v51
	v_mul_f32_e32 v0, 0x3fcc422a, v0
	v_mul_f32_e32 v0, 0xbfb8aa3b, v0
	v_exp_f32_e32 v0, v0
	s_nop 0
	v_add_f32_e32 v0, 1.0, v0
	v_rcp_f32_e32 v53, v0
	v_mul_f32_e32 v0, 0x3d372713, v42
	v_mul_f32_e32 v0, v42, v0
	v_fma_f32 v0, v42, v0, v42
	v_mul_f32_e32 v0, 0x3fcc422a, v0
	v_mul_f32_e32 v0, 0xbfb8aa3b, v0
	v_exp_f32_e32 v0, v0
	v_pk_mul_f32 v[70:71], v[50:51], v[52:53]
	v_cvt_pk_bf16_f32 v50, v58, v59
	v_add_co_u32_e32 v58, vcc, s6, v158
	v_cvt_pk_bf16_f32 v51, v60, v61
	v_cvt_pk_bf16_f32 v52, v64, v65
	v_cvt_pk_bf16_f32 v53, v70, v71
	v_addc_co_u32_e32 v59, vcc, 0, v159, vcc
	v_add_f32_e32 v0, 1.0, v0
	global_store_dwordx4 v[58:59], v[50:53], off
	s_mov_b64 s[6:7], 0x14000
	s_nop 0
	v_rcp_f32_e32 v50, v0
	v_mul_f32_e32 v0, 0x3d372713, v43
	v_mul_f32_e32 v0, v43, v0
	v_fma_f32 v0, v43, v0, v43
	v_mul_f32_e32 v0, 0x3fcc422a, v0
	v_mul_f32_e32 v0, 0xbfb8aa3b, v0
	v_exp_f32_e32 v0, v0
	s_nop 0
	v_add_f32_e32 v0, 1.0, v0
	v_rcp_f32_e32 v51, v0
	v_mul_f32_e32 v0, 0x3d372713, v44
	v_mul_f32_e32 v0, v44, v0
	v_fma_f32 v0, v44, v0, v44
	v_mul_f32_e32 v0, 0x3fcc422a, v0
	v_mul_f32_e32 v0, 0xbfb8aa3b, v0
	v_exp_f32_e32 v0, v0
	v_pk_mul_f32 v[42:43], v[42:43], v[50:51]
	v_add_f32_e32 v0, 1.0, v0
	v_rcp_f32_e32 v50, v0
	v_mul_f32_e32 v0, 0x3d372713, v45
	v_mul_f32_e32 v0, v45, v0
	v_fma_f32 v0, v45, v0, v45
	v_mul_f32_e32 v0, 0x3fcc422a, v0
	v_mul_f32_e32 v0, 0xbfb8aa3b, v0
	v_exp_f32_e32 v0, v0
	s_nop 0
	v_add_f32_e32 v0, 1.0, v0
	v_rcp_f32_e32 v51, v0
	v_mul_f32_e32 v0, 0x3d372713, v34
	v_mul_f32_e32 v0, v34, v0
	v_fma_f32 v0, v34, v0, v34
	v_mul_f32_e32 v0, 0x3fcc422a, v0
	v_mul_f32_e32 v0, 0xbfb8aa3b, v0
	v_exp_f32_e32 v0, v0
	v_pk_mul_f32 v[44:45], v[44:45], v[50:51]
	v_add_f32_e32 v0, 1.0, v0
	v_rcp_f32_e32 v50, v0
	v_mul_f32_e32 v0, 0x3d372713, v35
	v_mul_f32_e32 v0, v35, v0
	v_fma_f32 v0, v35, v0, v35
	v_mul_f32_e32 v0, 0x3fcc422a, v0
	v_mul_f32_e32 v0, 0xbfb8aa3b, v0
	v_exp_f32_e32 v0, v0
	s_nop 0
	v_add_f32_e32 v0, 1.0, v0
	v_rcp_f32_e32 v51, v0
	s_nop 0
	v_pk_mul_f32 v[50:51], v[34:35], v[50:51]
	v_pk_add_f32 v[34:35], v[36:37], v[40:41]
	s_nop 0
	v_mul_f32_e32 v0, 0x3d372713, v34
	v_mul_f32_e32 v0, v34, v0
	v_fma_f32 v0, v34, v0, v34
	v_mul_f32_e32 v0, 0x3fcc422a, v0
	v_mul_f32_e32 v0, 0xbfb8aa3b, v0
	v_exp_f32_e32 v0, v0
	s_nop 0
	v_add_f32_e32 v0, 1.0, v0
	v_rcp_f32_e32 v36, v0
	v_mul_f32_e32 v0, 0x3d372713, v35
	v_mul_f32_e32 v0, v35, v0
	v_fma_f32 v0, v35, v0, v35
	v_mul_f32_e32 v0, 0x3fcc422a, v0
	v_mul_f32_e32 v0, 0xbfb8aa3b, v0
	v_exp_f32_e32 v0, v0
	s_nop 0
	v_add_f32_e32 v0, 1.0, v0
	v_rcp_f32_e32 v37, v0
	v_mul_f32_e32 v0, 0x3d372713, v30
	v_mul_f32_e32 v0, v30, v0
	v_fma_f32 v0, v30, v0, v30
	v_mul_f32_e32 v0, 0x3fcc422a, v0
	v_mul_f32_e32 v0, 0xbfb8aa3b, v0
	v_exp_f32_e32 v0, v0
	v_pk_mul_f32 v[52:53], v[34:35], v[36:37]
	v_cvt_pk_bf16_f32 v34, v42, v43
	v_cvt_pk_bf16_f32 v35, v44, v45
	v_cvt_pk_bf16_f32 v36, v50, v51
	v_cvt_pk_bf16_f32 v37, v52, v53
	v_add_f32_e32 v0, 1.0, v0
	global_store_dwordx4 v[62:63], v[34:37], off offset:256
	s_nop 1
	v_rcp_f32_e32 v36, v0
	v_mul_f32_e32 v0, 0x3d372713, v31
	v_mul_f32_e32 v0, v31, v0
	v_fma_f32 v0, v31, v0, v31
	v_mul_f32_e32 v0, 0x3fcc422a, v0
	v_mul_f32_e32 v0, 0xbfb8aa3b, v0
	v_exp_f32_e32 v0, v0
	v_lshl_add_u64 v[34:35], v[158:159], 0, s[6:7]
	s_mov_b32 s6, 0x14000
	v_add_f32_e32 v0, 1.0, v0
	v_rcp_f32_e32 v37, v0
	v_mul_f32_e32 v0, 0x3d372713, v32
	v_mul_f32_e32 v0, v32, v0
	v_fma_f32 v0, v32, v0, v32
	v_mul_f32_e32 v0, 0x3fcc422a, v0
	v_mul_f32_e32 v0, 0xbfb8aa3b, v0
; __device__ __forceinline__ unsigned pk2(float lo, float hi) { const f32x2 f = {lo, hi}; const bf16n2 v = __builtin_convertvector(f, bf16n2); return __builtin_bit_cast(unsigned, v); }
; __device__ __forceinline__ float sigmoidf_(float x) { return __builtin_amdgcn_rcpf(1.0f + __expf(-x)); }
;     __device__ __forceinline__ bool operator()(f32x4 (&acc)[2][2][4][2], const Unit& u, int wr, int wc, int fr, int fq) const {
;     ...
;         for (int ai = 0; ai < 2; ++ai)
; #pragma unroll
;             for (int m = 0; m < 4; ++m) { bf16_t* rowp = hid + ((size_t)kv * 2048 + row0 + ai * HALF + m * 16) * 256 + col0;
; #pragma unroll
;                 for (int bj = 0; bj < 2; ++bj) { float o[8];
; #pragma unroll
;                     for (int j = 0; j < 8; ++j) { const float x = acc[ai][bj][m][j >> 2][j & 3] + bv[bj][j];
;                         o[j] = x * sigmoidf_(1.5957691216f * (x + 0.044715f * x * x * x)); }
;                     u32x4 w; w.x = pk2(o[0], o[1]); w.y = pk2(o[2], o[3]); w.z = pk2(o[4], o[5]); w.w = pk2(o[6], o[7]);
;                     *(u32x4*)(rowp + bj * HALF) = w; } }
	v_exp_f32_e32 v0, v0
	v_pk_mul_f32 v[30:31], v[30:31], v[36:37]
	v_add_f32_e32 v0, 1.0, v0
	v_rcp_f32_e32 v36, v0
	v_mul_f32_e32 v0, 0x3d372713, v33
	v_mul_f32_e32 v0, v33, v0
	v_fma_f32 v0, v33, v0, v33
	v_mul_f32_e32 v0, 0x3fcc422a, v0
	v_mul_f32_e32 v0, 0xbfb8aa3b, v0
	v_exp_f32_e32 v0, v0
	s_nop 0
	v_add_f32_e32 v0, 1.0, v0
	v_rcp_f32_e32 v37, v0
	v_mul_f32_e32 v0, 0x3d372713, v26
	v_mul_f32_e32 v0, v26, v0
	v_fma_f32 v0, v26, v0, v26
	v_mul_f32_e32 v0, 0x3fcc422a, v0
	v_mul_f32_e32 v0, 0xbfb8aa3b, v0
	v_exp_f32_e32 v0, v0
	v_pk_mul_f32 v[32:33], v[32:33], v[36:37]
	v_add_f32_e32 v0, 1.0, v0
	v_rcp_f32_e32 v36, v0
	v_mul_f32_e32 v0, 0x3d372713, v27
	v_mul_f32_e32 v0, v27, v0
	v_fma_f32 v0, v27, v0, v27
	v_mul_f32_e32 v0, 0x3fcc422a, v0
	v_mul_f32_e32 v0, 0xbfb8aa3b, v0
	v_exp_f32_e32 v0, v0
	s_nop 0
	v_add_f32_e32 v0, 1.0, v0
	v_rcp_f32_e32 v37, v0
	s_nop 0
	v_pk_mul_f32 v[36:37], v[26:27], v[36:37]
	v_pk_add_f32 v[26:27], v[28:29], v[48:49]
	s_nop 0
	v_mul_f32_e32 v0, 0x3d372713, v26
	v_mul_f32_e32 v0, v26, v0
	v_fma_f32 v0, v26, v0, v26
	v_mul_f32_e32 v0, 0x3fcc422a, v0
	v_mul_f32_e32 v0, 0xbfb8aa3b, v0
	v_exp_f32_e32 v0, v0
	s_nop 0
	v_add_f32_e32 v0, 1.0, v0
	v_rcp_f32_e32 v28, v0
	v_mul_f32_e32 v0, 0x3d372713, v27
	v_mul_f32_e32 v0, v27, v0
	v_fma_f32 v0, v27, v0, v27
	v_mul_f32_e32 v0, 0x3fcc422a, v0
	v_mul_f32_e32 v0, 0xbfb8aa3b, v0
	v_exp_f32_e32 v0, v0
	s_nop 0
	v_add_f32_e32 v0, 1.0, v0
	v_rcp_f32_e32 v29, v0
	v_mul_f32_e32 v0, 0x3d372713, v22
	v_mul_f32_e32 v0, v22, v0
	v_fma_f32 v0, v22, v0, v22
	v_mul_f32_e32 v0, 0x3fcc422a, v0
	v_mul_f32_e32 v0, 0xbfb8aa3b, v0
	v_exp_f32_e32 v0, v0
	v_pk_mul_f32 v[42:43], v[26:27], v[28:29]
	v_cvt_pk_bf16_f32 v26, v30, v31
	v_add_co_u32_e32 v30, vcc, s6, v158
	v_cvt_pk_bf16_f32 v27, v32, v33
	v_cvt_pk_bf16_f32 v28, v36, v37
	v_cvt_pk_bf16_f32 v29, v42, v43
	v_addc_co_u32_e32 v31, vcc, 0, v159, vcc
	v_add_f32_e32 v0, 1.0, v0
	global_store_dwordx4 v[30:31], v[26:29], off
	s_mov_b64 s[6:7], 0x16000
	s_nop 0
	v_rcp_f32_e32 v26, v0
	v_mul_f32_e32 v0, 0x3d372713, v23
	v_mul_f32_e32 v0, v23, v0
	v_fma_f32 v0, v23, v0, v23
	v_mul_f32_e32 v0, 0x3fcc422a, v0
	v_mul_f32_e32 v0, 0xbfb8aa3b, v0
	v_exp_f32_e32 v0, v0
	s_nop 0
	v_add_f32_e32 v0, 1.0, v0
	v_rcp_f32_e32 v27, v0
	v_mul_f32_e32 v0, 0x3d372713, v24
	v_mul_f32_e32 v0, v24, v0
	v_fma_f32 v0, v24, v0, v24
	v_mul_f32_e32 v0, 0x3fcc422a, v0
	v_mul_f32_e32 v0, 0xbfb8aa3b, v0
	v_exp_f32_e32 v0, v0
	v_pk_mul_f32 v[22:23], v[22:23], v[26:27]
	v_add_f32_e32 v0, 1.0, v0
	v_rcp_f32_e32 v26, v0
	v_mul_f32_e32 v0, 0x3d372713, v25
	v_mul_f32_e32 v0, v25, v0
	v_fma_f32 v0, v25, v0, v25
	v_mul_f32_e32 v0, 0x3fcc422a, v0
	v_mul_f32_e32 v0, 0xbfb8aa3b, v0
	v_exp_f32_e32 v0, v0
	s_nop 0
	v_add_f32_e32 v0, 1.0, v0
	v_rcp_f32_e32 v27, v0
	v_mul_f32_e32 v0, 0x3d372713, v18
	v_mul_f32_e32 v0, v18, v0
	v_fma_f32 v0, v18, v0, v18
	v_mul_f32_e32 v0, 0x3fcc422a, v0
	v_mul_f32_e32 v0, 0xbfb8aa3b, v0
	v_exp_f32_e32 v0, v0
	v_pk_mul_f32 v[24:25], v[24:25], v[26:27]
	v_add_f32_e32 v0, 1.0, v0
	v_rcp_f32_e32 v26, v0
	v_mul_f32_e32 v0, 0x3d372713, v19
	v_mul_f32_e32 v0, v19, v0
	v_fma_f32 v0, v19, v0, v19
	v_mul_f32_e32 v0, 0x3fcc422a, v0
	v_mul_f32_e32 v0, 0xbfb8aa3b, v0
	v_exp_f32_e32 v0, v0
	s_nop 0
	v_add_f32_e32 v0, 1.0, v0
	v_rcp_f32_e32 v27, v0
	s_nop 0
	v_pk_mul_f32 v[26:27], v[18:19], v[26:27]
	v_pk_add_f32 v[18:19], v[20:21], v[40:41]
	s_nop 0
	v_mul_f32_e32 v0, 0x3d372713, v18
	v_mul_f32_e32 v0, v18, v0
	v_fma_f32 v0, v18, v0, v18
	v_mul_f32_e32 v0, 0x3fcc422a, v0
	v_mul_f32_e32 v0, 0xbfb8aa3b, v0
	v_exp_f32_e32 v0, v0
	s_nop 0
	v_add_f32_e32 v0, 1.0, v0
	v_rcp_f32_e32 v20, v0
	v_mul_f32_e32 v0, 0x3d372713, v19
	v_mul_f32_e32 v0, v19, v0
	v_fma_f32 v0, v19, v0, v19
	v_mul_f32_e32 v0, 0x3fcc422a, v0
	v_mul_f32_e32 v0, 0xbfb8aa3b, v0
	v_exp_f32_e32 v0, v0
	s_nop 0
	v_add_f32_e32 v0, 1.0, v0
	v_rcp_f32_e32 v21, v0
	v_mul_f32_e32 v0, 0x3d372713, v14
	v_mul_f32_e32 v0, v14, v0
	v_fma_f32 v0, v14, v0, v14
	v_mul_f32_e32 v0, 0x3fcc422a, v0
	v_mul_f32_e32 v0, 0xbfb8aa3b, v0
	v_exp_f32_e32 v0, v0
	v_pk_mul_f32 v[28:29], v[18:19], v[20:21]
	v_cvt_pk_bf16_f32 v18, v22, v23
	v_cvt_pk_bf16_f32 v19, v24, v25
	v_cvt_pk_bf16_f32 v20, v26, v27
	v_cvt_pk_bf16_f32 v21, v28, v29
	v_add_f32_e32 v0, 1.0, v0
	global_store_dwordx4 v[34:35], v[18:21], off offset:256
	s_nop 1
	v_rcp_f32_e32 v20, v0
	v_mul_f32_e32 v0, 0x3d372713, v15
	v_mul_f32_e32 v0, v15, v0
	v_fma_f32 v0, v15, v0, v15
	v_mul_f32_e32 v0, 0x3fcc422a, v0
	v_mul_f32_e32 v0, 0xbfb8aa3b, v0
	v_exp_f32_e32 v0, v0
	v_lshl_add_u64 v[18:19], v[158:159], 0, s[6:7]
	s_mov_b32 s6, 0x16000
	v_add_f32_e32 v0, 1.0, v0
	v_rcp_f32_e32 v21, v0
	v_mul_f32_e32 v0, 0x3d372713, v16
	v_mul_f32_e32 v0, v16, v0
	v_fma_f32 v0, v16, v0, v16
	v_mul_f32_e32 v0, 0x3fcc422a, v0
	v_mul_f32_e32 v0, 0xbfb8aa3b, v0
	v_exp_f32_e32 v0, v0
	v_pk_mul_f32 v[14:15], v[14:15], v[20:21]
	v_add_f32_e32 v0, 1.0, v0
	v_rcp_f32_e32 v20, v0
	v_mul_f32_e32 v0, 0x3d372713, v17
	v_mul_f32_e32 v0, v17, v0
	v_fma_f32 v0, v17, v0, v17
	v_mul_f32_e32 v0, 0x3fcc422a, v0
	v_mul_f32_e32 v0, 0xbfb8aa3b, v0
	v_exp_f32_e32 v0, v0
	s_nop 0
	v_add_f32_e32 v0, 1.0, v0
	v_rcp_f32_e32 v21, v0
	v_mul_f32_e32 v0, 0x3d372713, v10
	v_mul_f32_e32 v0, v10, v0
	v_fma_f32 v0, v10, v0, v10
	v_mul_f32_e32 v0, 0x3fcc422a, v0
	v_mul_f32_e32 v0, 0xbfb8aa3b, v0
	v_exp_f32_e32 v0, v0
	v_pk_mul_f32 v[16:17], v[16:17], v[20:21]
	v_add_f32_e32 v0, 1.0, v0
	v_rcp_f32_e32 v20, v0
	v_mul_f32_e32 v0, 0x3d372713, v11
	v_mul_f32_e32 v0, v11, v0
	v_fma_f32 v0, v11, v0, v11
	v_mul_f32_e32 v0, 0x3fcc422a, v0
	v_mul_f32_e32 v0, 0xbfb8aa3b, v0
	v_exp_f32_e32 v0, v0
; __device__ __forceinline__ unsigned pk2(float lo, float hi) { const f32x2 f = {lo, hi}; const bf16n2 v = __builtin_convertvector(f, bf16n2); return __builtin_bit_cast(unsigned, v); }
; __device__ __forceinline__ float sigmoidf_(float x) { return __builtin_amdgcn_rcpf(1.0f + __expf(-x)); }
; #define PHASE_END   } if (gp + 1 < hi) xcd_barrier(bar); } ++gp;
; #define RELAUNDER() do { asm volatile("" : "+v"(pc.tid), "+s"(pc.bid)); pc.lane = pc.tid & 63; pc.wave = __builtin_amdgcn_readfirstlane(pc.tid >> 6); } while (0)
;     __device__ __forceinline__ bool operator()(f32x4 (&acc)[2][2][4][2], const Unit& u, int wr, int wc, int fr, int fq) const {
;     ...
;                 for (int bj = 0; bj < 2; ++bj) { float o[8];
; #pragma unroll
;                     for (int j = 0; j < 8; ++j) { const float x = acc[ai][bj][m][j >> 2][j & 3] + bv[bj][j];
;                         o[j] = x * sigmoidf_(1.5957691216f * (x + 0.044715f * x * x * x)); }
;                     u32x4 w; w.x = pk2(o[0], o[1]); w.y = pk2(o[2], o[3]); w.z = pk2(o[4], o[5]); w.w = pk2(o[6], o[7]);
;                     *(u32x4*)(rowp + bj * HALF) = w; } }
; __global__ void __launch_bounds__(512, 2) fwd_kernel(Args args) {
;     ...
;                 RELAUNDER();
;                 if (c.bid >= 16) { Ctx cv = c; cv.bid = c.bid - 16; cv.G = c.G - 16; phase_lora_a(cv, args, layer, proj, alora); vt_transpose(cv, proj, vtb); } } PHASE_END
	s_nop 0
	v_add_f32_e32 v0, 1.0, v0
	v_rcp_f32_e32 v21, v0
	s_nop 0
	v_pk_mul_f32 v[20:21], v[10:11], v[20:21]
	v_pk_add_f32 v[10:11], v[12:13], v[48:49]
	s_nop 0
	v_mul_f32_e32 v0, 0x3d372713, v10
	v_mul_f32_e32 v0, v10, v0
	v_fma_f32 v0, v10, v0, v10
	v_mul_f32_e32 v0, 0x3fcc422a, v0
	v_mul_f32_e32 v0, 0xbfb8aa3b, v0
	v_exp_f32_e32 v0, v0
	s_nop 0
	v_add_f32_e32 v0, 1.0, v0
	v_rcp_f32_e32 v12, v0
	v_mul_f32_e32 v0, 0x3d372713, v11
	v_mul_f32_e32 v0, v11, v0
	v_fma_f32 v0, v11, v0, v11
	v_mul_f32_e32 v0, 0x3fcc422a, v0
	v_mul_f32_e32 v0, 0xbfb8aa3b, v0
	v_exp_f32_e32 v0, v0
	s_nop 0
	v_add_f32_e32 v0, 1.0, v0
	v_rcp_f32_e32 v13, v0
	v_mul_f32_e32 v0, 0x3d372713, v6
	v_mul_f32_e32 v0, v6, v0
	v_fma_f32 v0, v6, v0, v6
	v_mul_f32_e32 v0, 0x3fcc422a, v0
	v_mul_f32_e32 v0, 0xbfb8aa3b, v0
	v_exp_f32_e32 v0, v0
	v_pk_mul_f32 v[22:23], v[10:11], v[12:13]
	v_cvt_pk_bf16_f32 v10, v14, v15
	v_add_co_u32_e32 v14, vcc, s6, v158
	v_cvt_pk_bf16_f32 v11, v16, v17
	v_cvt_pk_bf16_f32 v12, v20, v21
	v_cvt_pk_bf16_f32 v13, v22, v23
	v_addc_co_u32_e32 v15, vcc, 0, v159, vcc
	v_add_f32_e32 v0, 1.0, v0
	global_store_dwordx4 v[14:15], v[10:13], off
	s_and_b64 vcc, exec, s[0:1]
	s_mov_b64 s[6:7], s[4:5]
	v_rcp_f32_e32 v10, v0
	v_mul_f32_e32 v0, 0x3d372713, v7
	v_mul_f32_e32 v0, v7, v0
	v_fma_f32 v0, v7, v0, v7
	v_mul_f32_e32 v0, 0x3fcc422a, v0
	v_mul_f32_e32 v0, 0xbfb8aa3b, v0
	v_exp_f32_e32 v0, v0
	s_nop 0
	v_add_f32_e32 v0, 1.0, v0
	v_rcp_f32_e32 v11, v0
	v_mul_f32_e32 v0, 0x3d372713, v8
	v_mul_f32_e32 v0, v8, v0
	v_fma_f32 v0, v8, v0, v8
	v_mul_f32_e32 v0, 0x3fcc422a, v0
	v_mul_f32_e32 v0, 0xbfb8aa3b, v0
	v_exp_f32_e32 v0, v0
	v_pk_mul_f32 v[6:7], v[6:7], v[10:11]
	v_add_f32_e32 v0, 1.0, v0
	v_rcp_f32_e32 v10, v0
	v_mul_f32_e32 v0, 0x3d372713, v9
	v_mul_f32_e32 v0, v9, v0
	v_fma_f32 v0, v9, v0, v9
	v_mul_f32_e32 v0, 0x3fcc422a, v0
	v_mul_f32_e32 v0, 0xbfb8aa3b, v0
	v_exp_f32_e32 v0, v0
	s_nop 0
	v_add_f32_e32 v0, 1.0, v0
	v_rcp_f32_e32 v11, v0
	v_mul_f32_e32 v0, 0x3d372713, v2
	v_mul_f32_e32 v0, v2, v0
	v_fma_f32 v0, v2, v0, v2
	v_mul_f32_e32 v0, 0x3fcc422a, v0
	v_mul_f32_e32 v0, 0xbfb8aa3b, v0
	v_exp_f32_e32 v0, v0
	v_pk_mul_f32 v[8:9], v[8:9], v[10:11]
	v_add_f32_e32 v0, 1.0, v0
	v_rcp_f32_e32 v10, v0
	v_mul_f32_e32 v0, 0x3d372713, v3
	v_mul_f32_e32 v0, v3, v0
	v_fma_f32 v0, v3, v0, v3
	v_mul_f32_e32 v0, 0x3fcc422a, v0
	v_mul_f32_e32 v0, 0xbfb8aa3b, v0
	v_exp_f32_e32 v0, v0
	s_nop 0
	v_add_f32_e32 v0, 1.0, v0
	v_rcp_f32_e32 v11, v0
	s_nop 0
	v_pk_mul_f32 v[10:11], v[2:3], v[10:11]
	v_pk_add_f32 v[2:3], v[4:5], v[40:41]
	s_nop 0
	v_mul_f32_e32 v0, 0x3d372713, v2
	v_mul_f32_e32 v0, v2, v0
	v_fma_f32 v0, v2, v0, v2
	v_mul_f32_e32 v0, 0x3fcc422a, v0
	v_mul_f32_e32 v0, 0xbfb8aa3b, v0
	v_exp_f32_e32 v0, v0
	s_nop 0
	v_add_f32_e32 v0, 1.0, v0
	v_rcp_f32_e32 v4, v0
	v_mul_f32_e32 v0, 0x3d372713, v3
	v_mul_f32_e32 v0, v3, v0
	v_fma_f32 v0, v3, v0, v3
	v_mul_f32_e32 v0, 0x3fcc422a, v0
	v_mul_f32_e32 v0, 0xbfb8aa3b, v0
	v_exp_f32_e32 v0, v0
	s_nop 0
	v_add_f32_e32 v0, 1.0, v0
	v_rcp_f32_e32 v5, v0
	s_nop 0
	v_pk_mul_f32 v[12:13], v[2:3], v[4:5]
	v_cvt_pk_bf16_f32 v2, v6, v7
	v_cvt_pk_bf16_f32 v3, v8, v9
	v_cvt_pk_bf16_f32 v4, v10, v11
	v_cvt_pk_bf16_f32 v5, v12, v13
	global_store_dwordx4 v[18:19], v[2:5], off offset:256
	s_cbranch_vccz .LBB0_482
.Lsk_bdone:
	s_waitcnt vmcnt(0)
	s_cmpk_gt_u32 s15, 0xff
	s_cbranch_scc1 .LBB0_493
	s_barrier
.LBB0_493:
	s_barrier
	v_readlane_b32 s6, v251, 0
	s_sub_i32 s6, s6, 16
	s_cmp_lt_u32 s6, 16
	s_cbranch_scc0 .Lsk_noflag
	v_readlane_b32 s6, v251, 0
	s_and_b32 s6, s6, 15
	s_lshl_b32 s6, s6, 6
	s_addk_i32 s6, 0x4000
	v_readlane_b32 s11, v252, 29
	v_readlane_b32 s13, v252, 30
	s_add_u32 s11, s11, s6
	s_addc_u32 s13, s13, 0
	v_mov_b32_e32 v160, s11
	v_mov_b32_e32 v161, s13
	v_cmp_eq_u32_e32 vcc, 0, v151
	s_and_saveexec_b64 s[8:9], vcc
	v_mov_b32_e32 v159, 1
	global_atomic_add v[160:161], v159, off
	s_waitcnt vmcnt(0)
	s_or_b64 exec, exec, s[8:9]
.Lsk_noflag:
.LBB0_494:
	v_readlane_b32 s16, v252, 47
	s_cmp_lt_i32 s14, 32
	v_readlane_b32 s11, v252, 20
	v_readlane_b32 s12, v253, 43
	v_readlane_b32 s17, v252, 48
	v_readlane_b32 s13, v253, 44
	s_cbranch_scc1 .LBB0_503
	v_readlane_b32 s0, v253, 9
	v_readlane_b32 s1, v253, 10
	s_add_i32 s10, s14, -32
	v_mov_b32_e32 v0, s0
	ds_read_b32 v0, v0
	v_ashrrev_i32_e32 v11, 5, v151
	v_lshl_add_u32 v10, s10, 4, v11
	s_movk_i32 s2, 0x4000
	v_cmp_gt_i32_e32 vcc, s2, v10
	s_waitcnt lgkmcnt(0)
	v_readfirstlane_b32 s0, v0
	v_mov_b32_e32 v0, s1
	ds_read_b32 v0, v0
	s_waitcnt lgkmcnt(0)
	v_readfirstlane_b32 s1, v0
	s_and_saveexec_b64 s[4:5], vcc
	s_cbranch_execz .LBB0_500
	v_readlane_b32 s2, v254, 24
	s_add_u32 s0, s0, s2
	v_and_b32_e32 v12, 31, v151
	s_addc_u32 s1, s1, 0
	v_lshlrev_b32_e32 v0, 5, v12
	v_lshl_add_u64 v[2:3], s[0:1], 0, v[0:1]
	v_add_co_u32_e32 v6, vcc, 0x1000, v2
	v_lshl_add_u32 v11, s14, 4, v11
	s_nop 0
	v_addc_co_u32_e32 v7, vcc, 0, v3, vcc
	flat_load_dwordx4 v[2:5], v[6:7] offset:2048
	s_nop 0
	flat_load_dwordx4 v[6:9], v[6:7] offset:2064
	v_add_u32_e32 v20, 0xfffffdff, v11
	v_ashrrev_i32_e32 v11, 31, v10
	v_lshlrev_b32_e32 v0, 4, v12
	v_cmp_gt_u32_e32 vcc, 8, v12
	v_cmp_gt_u32_e64 s[0:1], 16, v12
	v_lshlrev_b64 v[12:13], 9, v[10:11]
	v_readlane_b32 s2, v252, 18
	v_or_b32_e32 v12, v12, v0
	v_readlane_b32 s3, v252, 19
	v_lshlrev_b64 v[10:11], 13, v[10:11]
	v_or_b32_e32 v10, v10, v0
	v_lshl_add_u64 v[16:17], s[2:3], 0, v[12:13]
	v_readlane_b32 s2, v252, 49
	v_readlane_b32 s3, v252, 50
	v_lshl_add_u64 v[14:15], s[80:81], 0, v[0:1]
	s_mov_b64 s[6:7], 0
	v_lshl_add_u64 v[18:19], s[2:3], 0, v[10:11]
	v_mov_b32_e32 v0, v20
	s_branch .LBB0_498

; #define LAS __attribute__((address_space(3)))
; #define PHASE_END   } if (gp + 1 < hi) xcd_barrier(bar); } ++gp;
; __device__ __forceinline__ void vt_transpose(const Ctx& c, const bf16_t* proj, bf16_t* vt) {
;     ...
;     for (int it = c.bid; it < 3 * 2 * 256; it += c.G) {
;         const int which = it / 512, g = (it >> 8) & 1, tt = it & 255;
;         const int col = (which == 0 ? PC_VS : (which == 1 ? PC_VW : PC_SV)) + g * 64;
;         { const int tok = c.tid >> 3, ch = c.tid & 7; const u32x4 w = *(const u32x4*)(proj + (size_t)(tt * 64 + tok) * PLD + col + ch * 8);
;           *(LAS u32x4*)(tl + tok * 72 + ch * 8) = w; }
; __global__ void __launch_bounds__(512, 2) fwd_kernel(Args args) {
;     ...
;                 if (c.bid >= 16) { Ctx cv = c; cv.bid = c.bid - 16; cv.G = c.G - 16; phase_lora_a(cv, args, layer, proj, alora); vt_transpose(cv, proj, vtb); } } PHASE_END
.LBB0_500:
	s_or_b64 exec, exec, s[4:5]
	s_cmpk_gt_i32 s14, 0x61f
	s_cbranch_scc1 .LBB0_503
	v_ashrrev_i32_e32 v2, 3, v151
	v_mul_lo_u32 v3, v2, s67
	v_lshlrev_b32_e32 v0, 3, v151
	v_add_u32_e32 v4, 0, v3
	s_movk_i32 s0, 0xff72
	v_and_b32_e32 v0, 56, v0
	v_mad_u64_u32 v[8:9], s[0:1], v2, s0, v[4:5]
	v_ashrrev_i32_e32 v3, 31, v2
	v_lshl_add_u32 v6, v0, 1, v4
	v_mul_u32_u24_e32 v7, 0x90, v0
	v_lshlrev_b64 v[4:5], 15, v[2:3]
	s_lshl_b32 s0, s14, 6
	v_lshl_add_u64 v[4:5], s[82:83], 0, v[4:5]
	s_addk_i32 s0, 0xf800
	v_lshlrev_b32_e32 v0, 1, v0
	v_add_u32_e32 v3, v8, v7
	v_readlane_b32 s5, v252, 52
	s_mov_b32 s6, 0x5040100
